# GEMM K-loops: in the 8-read load sections the stage pieces are issued before the fragment reads
# speedup vs baseline: 1.0005x; 1.0005x over previous
.LBB0_243:
	s_add_u32 s75, s6, 0x100
	s_addc_u32 s48, s7, 0
	s_lshl_b32 s49, s45, 8
	s_lshl_b32 s8, s45, 20
	s_bitset1_b32 s49, 7
	s_mov_b32 s80, -2
	s_mov_b64 s[6:7], 0
	s_cmp_eq_u32 s80, 28
	s_cselect_b64 s[34:35], -1, 0
	s_and_b64 s[24:25], s[0:1], s[34:35]
	s_andn2_b64 vcc, exec, s[24:25]
	v_mov_b32_e32 v128, v170
	v_mov_b32_e32 v129, v160
	s_add_u32 vcc_lo, s70, s6
	s_addc_u32 vcc_hi, s71, s7
	s_add_u32 s81, vcc_lo, 0x32000100
	s_addc_u32 s50, vcc_hi, 0
	s_and_b64 s[24:25], s[34:35], exec
	s_cselect_b32 s25, s73, s50
	s_cselect_b32 s24, s72, s81
	s_add_u32 s50, s75, s6
	s_addc_u32 s51, s48, s7
	s_and_b64 s[34:35], s[34:35], exec
	s_cselect_b32 s35, s79, s51
	s_cselect_b32 s34, s78, s50
	s_add_i32 s50, 0, 0x10000
	s_add_i32 s51, 0, 0x14000
	v_add_u32_e32 v142, s50, v177
	v_add_u32_e32 v158, s51, v177
	ds_read_b128 v[130:133], v142
	ds_read_b128 v[134:137], v213
	ds_read_b128 v[138:141], v142 offset:2048
	ds_read_b128 v[142:145], v213 offset:2048
	ds_read_b128 v[146:149], v158
	ds_read_b128 v[150:153], v213 offset:16384
	ds_read_b128 v[154:157], v158 offset:2048
	ds_read_b128 v[172:175], v213 offset:18432
	ds_read_b128 v[180:183], v178
	ds_read_b128 v[184:187], v212
	ds_read_b128 v[188:191], v178 offset:2048
	ds_read_b128 v[192:195], v212 offset:2048
	ds_read_b128 v[196:199], v178 offset:4096
	ds_read_b128 v[200:203], v212 offset:4096
	ds_read_b128 v[204:207], v178 offset:6144
	ds_read_b128 v[208:211], v212 offset:6144
	s_add_i32 m0, s97, 0xc000
	s_add_u32 vcc_lo, vcc_lo, s54
	s_addc_u32 vcc_hi, vcc_hi, s55
	v_mov_b32_e32 v171, v161
	global_load_lds_dwordx4 v160, vcc
	s_add_i32 m0, s97, 0xe000
	s_nop 0
	global_load_lds_dwordx4 v170, vcc
	s_waitcnt vmcnt(8)
	s_waitcnt lgkmcnt(0)
	s_barrier
	s_setprio 1
	s_waitcnt lgkmcnt(0)
	v_mfma_f32_16x16x32_bf16 v[100:103], v[130:133], v[180:183], 0
	v_mfma_f32_16x16x32_bf16 v[96:99], v[138:141], v[180:183], 0
	v_mfma_f32_16x16x32_bf16 v[92:95], v[130:133], v[188:191], 0
	v_mfma_f32_16x16x32_bf16 v[88:91], v[138:141], v[188:191], 0
	v_mfma_f32_16x16x32_bf16 v[84:87], v[130:133], v[196:199], 0
	v_mfma_f32_16x16x32_bf16 v[80:83], v[138:141], v[196:199], 0
	v_mfma_f32_16x16x32_bf16 v[76:79], v[130:133], v[204:207], 0
	v_mfma_f32_16x16x32_bf16 v[72:75], v[138:141], v[204:207], 0
	v_mfma_f32_16x16x32_bf16 v[100:103], v[134:137], v[184:187], v[100:103]
	v_mfma_f32_16x16x32_bf16 v[96:99], v[142:145], v[184:187], v[96:99]
	v_mfma_f32_16x16x32_bf16 v[92:95], v[134:137], v[192:195], v[92:95]
	v_mfma_f32_16x16x32_bf16 v[88:91], v[142:145], v[192:195], v[88:91]
	v_mfma_f32_16x16x32_bf16 v[84:87], v[134:137], v[200:203], v[84:87]
	v_mfma_f32_16x16x32_bf16 v[80:83], v[142:145], v[200:203], v[80:83]
	v_mfma_f32_16x16x32_bf16 v[76:79], v[134:137], v[208:211], v[76:79]
	v_mfma_f32_16x16x32_bf16 v[72:75], v[142:145], v[208:211], v[72:75]
	s_setprio 0
	s_setprio 1
	v_mfma_f32_16x16x32_bf16 v[68:71], v[146:149], v[180:183], 0
	v_mfma_f32_16x16x32_bf16 v[64:67], v[154:157], v[180:183], 0
	v_mfma_f32_16x16x32_bf16 v[60:63], v[146:149], v[188:191], 0
	v_mfma_f32_16x16x32_bf16 v[56:59], v[154:157], v[188:191], 0
	v_mfma_f32_16x16x32_bf16 v[52:55], v[146:149], v[196:199], 0
	v_mfma_f32_16x16x32_bf16 v[48:51], v[154:157], v[196:199], 0
	v_mfma_f32_16x16x32_bf16 v[40:43], v[146:149], v[204:207], 0
	v_mfma_f32_16x16x32_bf16 v[32:35], v[154:157], v[204:207], 0
	v_mfma_f32_16x16x32_bf16 v[68:71], v[150:153], v[184:187], v[68:71]
	v_mfma_f32_16x16x32_bf16 v[64:67], v[172:175], v[184:187], v[64:67]
	v_mfma_f32_16x16x32_bf16 v[60:63], v[150:153], v[192:195], v[60:63]
	v_mfma_f32_16x16x32_bf16 v[56:59], v[172:175], v[192:195], v[56:59]
	v_mfma_f32_16x16x32_bf16 v[52:55], v[150:153], v[200:203], v[52:55]
	v_mfma_f32_16x16x32_bf16 v[48:51], v[172:175], v[200:203], v[48:51]
	v_mfma_f32_16x16x32_bf16 v[40:43], v[150:153], v[208:211], v[40:43]
	v_mfma_f32_16x16x32_bf16 v[32:35], v[172:175], v[208:211], v[32:35]
	s_setprio 0
	s_barrier
	s_add_i32 s50, s50, s61
	s_mov_b32 m0, s50
	s_nop 0
	global_load_lds_dwordx4 v168, s[34:35]
	s_add_i32 m0, s50, 0x2000
	s_add_u32 vcc_lo, s34, 0x8000
	s_addc_u32 vcc_hi, s35, 0
	s_add_i32 s50, s51, s61
	s_nop 0
	global_load_lds_dwordx4 v162, s[34:35]
	s_mov_b32 m0, s50
	s_nop 0
	global_load_lds_dwordx4 v168, vcc
	s_add_i32 m0, s50, 0x2000
	s_nop 0
	global_load_lds_dwordx4 v162, vcc
	ds_read_b128 v[180:183], v178 offset:16384
	ds_read_b128 v[184:187], v212 offset:16384
	ds_read_b128 v[188:191], v178 offset:18432
	ds_read_b128 v[192:195], v212 offset:18432
	ds_read_b128 v[196:199], v178 offset:20480
	ds_read_b128 v[200:203], v212 offset:20480
	ds_read_b128 v[204:207], v178 offset:22528
	ds_read_b128 v[208:211], v212 offset:22528
	s_waitcnt vmcnt(6)
	s_waitcnt lgkmcnt(0)
	s_barrier
	s_setprio 1
	s_waitcnt lgkmcnt(0)
	v_mfma_f32_16x16x32_bf16 v[44:47], v[130:133], v[180:183], 0
	v_mfma_f32_16x16x32_bf16 v[36:39], v[138:141], v[180:183], 0
	v_mfma_f32_16x16x32_bf16 v[28:31], v[130:133], v[188:191], 0
	v_mfma_f32_16x16x32_bf16 v[24:27], v[138:141], v[188:191], 0
	v_mfma_f32_16x16x32_bf16 v[20:23], v[130:133], v[196:199], 0
	v_mfma_f32_16x16x32_bf16 v[16:19], v[138:141], v[196:199], 0
	v_mfma_f32_16x16x32_bf16 v[12:15], v[130:133], v[204:207], 0
	v_mfma_f32_16x16x32_bf16 v[8:11], v[138:141], v[204:207], 0
	v_mfma_f32_16x16x32_bf16 v[44:47], v[134:137], v[184:187], v[44:47]
	v_mfma_f32_16x16x32_bf16 v[36:39], v[142:145], v[184:187], v[36:39]
	v_mfma_f32_16x16x32_bf16 v[28:31], v[134:137], v[192:195], v[28:31]
	v_mfma_f32_16x16x32_bf16 v[24:27], v[142:145], v[192:195], v[24:27]
	v_mfma_f32_16x16x32_bf16 v[20:23], v[134:137], v[200:203], v[20:23]
	v_mfma_f32_16x16x32_bf16 v[16:19], v[142:145], v[200:203], v[16:19]
	v_mfma_f32_16x16x32_bf16 v[12:15], v[134:137], v[208:211], v[12:15]
	v_mfma_f32_16x16x32_bf16 v[8:11], v[142:145], v[208:211], v[8:11]
	s_setprio 0
	s_setprio 1
	v_mfma_f32_16x16x32_bf16 v[4:7], v[146:149], v[180:183], 0
	v_mfma_f32_16x16x32_bf16 v[0:3], v[154:157], v[180:183], 0
	v_mfma_f32_16x16x32_bf16 v[104:107], v[146:149], v[188:191], 0
	v_mfma_f32_16x16x32_bf16 v[108:111], v[154:157], v[188:191], 0
	v_mfma_f32_16x16x32_bf16 v[112:115], v[146:149], v[196:199], 0
	v_mfma_f32_16x16x32_bf16 v[116:119], v[154:157], v[196:199], 0
	v_mfma_f32_16x16x32_bf16 v[120:123], v[146:149], v[204:207], 0
	v_mfma_f32_16x16x32_bf16 v[124:127], v[154:157], v[204:207], 0
	v_mfma_f32_16x16x32_bf16 v[4:7], v[150:153], v[184:187], v[4:7]
	v_mfma_f32_16x16x32_bf16 v[0:3], v[172:175], v[184:187], v[0:3]
	v_mfma_f32_16x16x32_bf16 v[104:107], v[150:153], v[192:195], v[104:107]
	v_mfma_f32_16x16x32_bf16 v[108:111], v[172:175], v[192:195], v[108:111]
	v_mfma_f32_16x16x32_bf16 v[112:115], v[150:153], v[200:203], v[112:115]
	v_mfma_f32_16x16x32_bf16 v[116:119], v[172:175], v[200:203], v[116:119]
	v_mfma_f32_16x16x32_bf16 v[120:123], v[150:153], v[208:211], v[120:123]
	v_mfma_f32_16x16x32_bf16 v[124:127], v[172:175], v[208:211], v[124:127]
	s_setprio 0
	s_barrier
	s_add_i32 s50, 0, 0x18000
	s_add_i32 s51, 0, 0x1c000
	v_add_u32_e32 v142, s50, v177
	v_add_u32_e32 v158, s51, v177
	ds_read_b128 v[130:133], v142
	ds_read_b128 v[134:137], v213 offset:32768
	ds_read_b128 v[138:141], v142 offset:2048
	ds_read_b128 v[142:145], v213 offset:34816
	ds_read_b128 v[146:149], v158
	ds_read_b128 v[150:153], v213 offset:49152
	ds_read_b128 v[154:157], v158 offset:2048
	ds_read_b128 v[172:175], v213 offset:51200
	s_mov_b32 m0, s29
	v_mov_b32_e32 v160, v129
	ds_read_b128 v[180:183], v178 offset:32768
	ds_read_b128 v[184:187], v212 offset:32768
	ds_read_b128 v[188:191], v178 offset:34816
	ds_read_b128 v[192:195], v212 offset:34816
	ds_read_b128 v[196:199], v178 offset:36864
	ds_read_b128 v[200:203], v212 offset:36864
	ds_read_b128 v[204:207], v178 offset:38912
	ds_read_b128 v[208:211], v212 offset:38912
	s_mov_b32 m0, s97
	s_nop 0
	global_load_lds_dwordx4 v164, s[24:25]
	s_mov_b32 m0, s28
	s_nop 0
	global_load_lds_dwordx4 v166, s[24:25]
	s_mov_b32 m0, s29
	v_mov_b32_e32 v170, v128
	global_load_lds_dwordx4 v160, s[24:25]
	s_mov_b32 m0, s30
	s_nop 0
	global_load_lds_dwordx4 v170, s[24:25]
	s_waitcnt vmcnt(8)
	s_waitcnt lgkmcnt(0)
	s_barrier
	s_setprio 1
	s_waitcnt lgkmcnt(0)
	v_mfma_f32_16x16x32_bf16 v[100:103], v[130:133], v[180:183], v[100:103]
	v_mfma_f32_16x16x32_bf16 v[96:99], v[138:141], v[180:183], v[96:99]
	v_mfma_f32_16x16x32_bf16 v[92:95], v[130:133], v[188:191], v[92:95]
	v_mfma_f32_16x16x32_bf16 v[88:91], v[138:141], v[188:191], v[88:91]
	v_mfma_f32_16x16x32_bf16 v[84:87], v[130:133], v[196:199], v[84:87]
	v_mfma_f32_16x16x32_bf16 v[80:83], v[138:141], v[196:199], v[80:83]
	v_mfma_f32_16x16x32_bf16 v[76:79], v[130:133], v[204:207], v[76:79]
	v_mfma_f32_16x16x32_bf16 v[72:75], v[138:141], v[204:207], v[72:75]
	v_mfma_f32_16x16x32_bf16 v[100:103], v[134:137], v[184:187], v[100:103]
	v_mfma_f32_16x16x32_bf16 v[96:99], v[142:145], v[184:187], v[96:99]
	v_mfma_f32_16x16x32_bf16 v[92:95], v[134:137], v[192:195], v[92:95]
	v_mfma_f32_16x16x32_bf16 v[88:91], v[142:145], v[192:195], v[88:91]
	v_mfma_f32_16x16x32_bf16 v[84:87], v[134:137], v[200:203], v[84:87]
	v_mfma_f32_16x16x32_bf16 v[80:83], v[142:145], v[200:203], v[80:83]
	v_mfma_f32_16x16x32_bf16 v[76:79], v[134:137], v[208:211], v[76:79]
	v_mfma_f32_16x16x32_bf16 v[72:75], v[142:145], v[208:211], v[72:75]
	s_setprio 0
	s_setprio 1
	v_mfma_f32_16x16x32_bf16 v[68:71], v[146:149], v[180:183], v[68:71]
	v_mfma_f32_16x16x32_bf16 v[64:67], v[154:157], v[180:183], v[64:67]
	v_mfma_f32_16x16x32_bf16 v[60:63], v[146:149], v[188:191], v[60:63]
	v_mfma_f32_16x16x32_bf16 v[56:59], v[154:157], v[188:191], v[56:59]
	v_mfma_f32_16x16x32_bf16 v[52:55], v[146:149], v[196:199], v[52:55]
	v_mfma_f32_16x16x32_bf16 v[48:51], v[154:157], v[196:199], v[48:51]
	v_mfma_f32_16x16x32_bf16 v[40:43], v[146:149], v[204:207], v[40:43]
	v_mfma_f32_16x16x32_bf16 v[32:35], v[154:157], v[204:207], v[32:35]
	v_mfma_f32_16x16x32_bf16 v[68:71], v[150:153], v[184:187], v[68:71]
	v_mfma_f32_16x16x32_bf16 v[64:67], v[172:175], v[184:187], v[64:67]
	v_mfma_f32_16x16x32_bf16 v[60:63], v[150:153], v[192:195], v[60:63]
	v_mfma_f32_16x16x32_bf16 v[56:59], v[172:175], v[192:195], v[56:59]
	v_mfma_f32_16x16x32_bf16 v[52:55], v[150:153], v[200:203], v[52:55]
	v_mfma_f32_16x16x32_bf16 v[48:51], v[172:175], v[200:203], v[48:51]
	v_mfma_f32_16x16x32_bf16 v[40:43], v[150:153], v[208:211], v[40:43]
	v_mfma_f32_16x16x32_bf16 v[32:35], v[172:175], v[208:211], v[32:35]
	s_setprio 0
	s_barrier
	v_mov_b32_e32 v169, v161
	s_add_i32 s50, s50, s61
	s_add_u32 vcc_lo, s34, s52
	s_addc_u32 vcc_hi, s35, s53
	s_mov_b32 m0, s50
	v_mov_b32_e32 v163, v161
	global_load_lds_dwordx4 v168, vcc
	s_add_i32 m0, s50, 0x2000
	v_mov_b32_e32 v165, v161
	s_add_u32 s34, s34, 0x8080
	s_addc_u32 s35, s35, 0
	s_add_i32 s50, s51, s61
	global_load_lds_dwordx4 v162, vcc
	s_mov_b32 m0, s50
	v_mov_b32_e32 v167, v161
	global_load_lds_dwordx4 v168, s[34:35]
	s_add_i32 m0, s50, 0x2000
	s_nop 0
	global_load_lds_dwordx4 v162, s[34:35]
	s_mov_b32 m0, s31
	s_add_u32 vcc_lo, s24, s52
	s_addc_u32 vcc_hi, s25, s53
	global_load_lds_dwordx4 v164, vcc
	s_mov_b32 m0, s42
	s_nop 0
	global_load_lds_dwordx4 v166, vcc
	ds_read_b128 v[180:183], v178 offset:49152
	ds_read_b128 v[184:187], v212 offset:49152
	ds_read_b128 v[188:191], v178 offset:51200
	ds_read_b128 v[192:195], v212 offset:51200
	ds_read_b128 v[196:199], v178 offset:53248
	ds_read_b128 v[200:203], v212 offset:53248
	ds_read_b128 v[204:207], v178 offset:55296
	ds_read_b128 v[208:211], v212 offset:55296
	s_waitcnt vmcnt(8)
	s_waitcnt lgkmcnt(0)
	s_barrier
	s_setprio 1
	s_waitcnt lgkmcnt(0)
	v_mfma_f32_16x16x32_bf16 v[44:47], v[130:133], v[180:183], v[44:47]
	v_mfma_f32_16x16x32_bf16 v[36:39], v[138:141], v[180:183], v[36:39]
	v_mfma_f32_16x16x32_bf16 v[28:31], v[130:133], v[188:191], v[28:31]
	v_mfma_f32_16x16x32_bf16 v[24:27], v[138:141], v[188:191], v[24:27]
	v_mfma_f32_16x16x32_bf16 v[20:23], v[130:133], v[196:199], v[20:23]
	v_mfma_f32_16x16x32_bf16 v[16:19], v[138:141], v[196:199], v[16:19]
	v_mfma_f32_16x16x32_bf16 v[12:15], v[130:133], v[204:207], v[12:15]
	v_mfma_f32_16x16x32_bf16 v[8:11], v[138:141], v[204:207], v[8:11]
	v_mfma_f32_16x16x32_bf16 v[44:47], v[134:137], v[184:187], v[44:47]
	v_mfma_f32_16x16x32_bf16 v[36:39], v[142:145], v[184:187], v[36:39]
	v_mfma_f32_16x16x32_bf16 v[28:31], v[134:137], v[192:195], v[28:31]
	v_mfma_f32_16x16x32_bf16 v[24:27], v[142:145], v[192:195], v[24:27]
	v_mfma_f32_16x16x32_bf16 v[20:23], v[134:137], v[200:203], v[20:23]
	v_mfma_f32_16x16x32_bf16 v[16:19], v[142:145], v[200:203], v[16:19]
	v_mfma_f32_16x16x32_bf16 v[12:15], v[134:137], v[208:211], v[12:15]
	v_mfma_f32_16x16x32_bf16 v[8:11], v[142:145], v[208:211], v[8:11]
	s_setprio 0
	s_setprio 1
	v_mfma_f32_16x16x32_bf16 v[4:7], v[146:149], v[180:183], v[4:7]
	v_mfma_f32_16x16x32_bf16 v[0:3], v[154:157], v[180:183], v[0:3]
	v_mfma_f32_16x16x32_bf16 v[104:107], v[146:149], v[188:191], v[104:107]
	v_mfma_f32_16x16x32_bf16 v[108:111], v[154:157], v[188:191], v[108:111]
	v_mfma_f32_16x16x32_bf16 v[112:115], v[146:149], v[196:199], v[112:115]
	v_mfma_f32_16x16x32_bf16 v[116:119], v[154:157], v[196:199], v[116:119]
	v_mfma_f32_16x16x32_bf16 v[120:123], v[146:149], v[204:207], v[120:123]
	v_mfma_f32_16x16x32_bf16 v[124:127], v[154:157], v[204:207], v[124:127]
	v_mfma_f32_16x16x32_bf16 v[4:7], v[150:153], v[184:187], v[4:7]
	v_mfma_f32_16x16x32_bf16 v[0:3], v[172:175], v[184:187], v[0:3]
	v_mfma_f32_16x16x32_bf16 v[104:107], v[150:153], v[192:195], v[104:107]
	v_mfma_f32_16x16x32_bf16 v[108:111], v[172:175], v[192:195], v[108:111]
	v_mfma_f32_16x16x32_bf16 v[112:115], v[150:153], v[200:203], v[112:115]
	v_mfma_f32_16x16x32_bf16 v[116:119], v[172:175], v[200:203], v[116:119]
	v_mfma_f32_16x16x32_bf16 v[120:123], v[150:153], v[208:211], v[120:123]
	v_mfma_f32_16x16x32_bf16 v[124:127], v[172:175], v[208:211], v[124:127]
	s_setprio 0
	s_barrier
	s_add_i32 s80, s80, 2
	s_add_u32 s6, s6, 0x100
	s_addc_u32 s7, s7, 0
	s_branch .LBB0_245
.LBB0_244:
	s_add_u32 vcc_lo, s70, s6
	s_addc_u32 vcc_hi, s71, s7
	s_add_u32 s81, vcc_lo, 0x32000100
	s_addc_u32 s50, vcc_hi, 0
	s_and_b64 s[24:25], s[34:35], exec
	s_cselect_b32 s25, s73, s50
	s_cselect_b32 s24, s72, s81
	s_add_u32 s50, s75, s6
	s_addc_u32 s51, s48, s7
	s_and_b64 s[34:35], s[34:35], exec
	s_cselect_b32 s35, s79, s51
	s_cselect_b32 s34, s78, s50
	s_add_i32 s50, 0, 0x10000
	s_add_i32 s51, 0, 0x14000
	v_add_u32_e32 v142, s50, v177
	v_add_u32_e32 v158, s51, v177
	ds_read_b128 v[130:133], v142
	ds_read_b128 v[134:137], v213
	ds_read_b128 v[138:141], v142 offset:2048
	ds_read_b128 v[142:145], v213 offset:2048
	ds_read_b128 v[146:149], v158
	ds_read_b128 v[150:153], v213 offset:16384
	ds_read_b128 v[154:157], v158 offset:2048
	ds_read_b128 v[172:175], v213 offset:18432
	ds_read_b128 v[180:183], v178
	ds_read_b128 v[184:187], v212
	ds_read_b128 v[188:191], v178 offset:2048
	ds_read_b128 v[192:195], v212 offset:2048
	ds_read_b128 v[196:199], v178 offset:4096
	ds_read_b128 v[200:203], v212 offset:4096
	ds_read_b128 v[204:207], v178 offset:6144
	ds_read_b128 v[208:211], v212 offset:6144
	s_add_i32 m0, s97, 0xc000
	s_add_u32 vcc_lo, vcc_lo, s54
	s_addc_u32 vcc_hi, vcc_hi, s55
	v_mov_b32_e32 v171, v161
	global_load_lds_dwordx4 v160, vcc
	s_add_i32 m0, s97, 0xe000
	s_nop 0
	global_load_lds_dwordx4 v170, vcc
	s_waitcnt vmcnt(8)
	s_waitcnt lgkmcnt(0)
	s_barrier
	s_setprio 1
	s_waitcnt lgkmcnt(0)
	v_mfma_f32_16x16x32_bf16 v[100:103], v[130:133], v[180:183], v[100:103]
	v_mfma_f32_16x16x32_bf16 v[96:99], v[138:141], v[180:183], v[96:99]
	v_mfma_f32_16x16x32_bf16 v[92:95], v[130:133], v[188:191], v[92:95]
	v_mfma_f32_16x16x32_bf16 v[88:91], v[138:141], v[188:191], v[88:91]
	v_mfma_f32_16x16x32_bf16 v[84:87], v[130:133], v[196:199], v[84:87]
	v_mfma_f32_16x16x32_bf16 v[80:83], v[138:141], v[196:199], v[80:83]
	v_mfma_f32_16x16x32_bf16 v[76:79], v[130:133], v[204:207], v[76:79]
	v_mfma_f32_16x16x32_bf16 v[72:75], v[138:141], v[204:207], v[72:75]
	v_mfma_f32_16x16x32_bf16 v[100:103], v[134:137], v[184:187], v[100:103]
	v_mfma_f32_16x16x32_bf16 v[96:99], v[142:145], v[184:187], v[96:99]
	v_mfma_f32_16x16x32_bf16 v[92:95], v[134:137], v[192:195], v[92:95]
	v_mfma_f32_16x16x32_bf16 v[88:91], v[142:145], v[192:195], v[88:91]
	v_mfma_f32_16x16x32_bf16 v[84:87], v[134:137], v[200:203], v[84:87]
	v_mfma_f32_16x16x32_bf16 v[80:83], v[142:145], v[200:203], v[80:83]
	v_mfma_f32_16x16x32_bf16 v[76:79], v[134:137], v[208:211], v[76:79]
	v_mfma_f32_16x16x32_bf16 v[72:75], v[142:145], v[208:211], v[72:75]
	s_setprio 0
	s_setprio 1
	v_mfma_f32_16x16x32_bf16 v[68:71], v[146:149], v[180:183], v[68:71]
	v_mfma_f32_16x16x32_bf16 v[64:67], v[154:157], v[180:183], v[64:67]
	v_mfma_f32_16x16x32_bf16 v[60:63], v[146:149], v[188:191], v[60:63]
	v_mfma_f32_16x16x32_bf16 v[56:59], v[154:157], v[188:191], v[56:59]
	v_mfma_f32_16x16x32_bf16 v[52:55], v[146:149], v[196:199], v[52:55]
	v_mfma_f32_16x16x32_bf16 v[48:51], v[154:157], v[196:199], v[48:51]
	v_mfma_f32_16x16x32_bf16 v[40:43], v[146:149], v[204:207], v[40:43]
	v_mfma_f32_16x16x32_bf16 v[32:35], v[154:157], v[204:207], v[32:35]
	v_mfma_f32_16x16x32_bf16 v[68:71], v[150:153], v[184:187], v[68:71]
	v_mfma_f32_16x16x32_bf16 v[64:67], v[172:175], v[184:187], v[64:67]
	v_mfma_f32_16x16x32_bf16 v[60:63], v[150:153], v[192:195], v[60:63]
	v_mfma_f32_16x16x32_bf16 v[56:59], v[172:175], v[192:195], v[56:59]
	v_mfma_f32_16x16x32_bf16 v[52:55], v[150:153], v[200:203], v[52:55]
	v_mfma_f32_16x16x32_bf16 v[48:51], v[172:175], v[200:203], v[48:51]
	v_mfma_f32_16x16x32_bf16 v[40:43], v[150:153], v[208:211], v[40:43]
	v_mfma_f32_16x16x32_bf16 v[32:35], v[172:175], v[208:211], v[32:35]
	s_setprio 0
	s_barrier
	s_add_i32 s50, s50, s61
	s_mov_b32 m0, s50
	s_nop 0
	global_load_lds_dwordx4 v168, s[34:35]
	s_add_i32 m0, s50, 0x2000
	s_add_u32 vcc_lo, s34, 0x8000
	s_addc_u32 vcc_hi, s35, 0
	s_add_i32 s50, s51, s61
	s_nop 0
	global_load_lds_dwordx4 v162, s[34:35]
	s_mov_b32 m0, s50
	s_nop 0
	global_load_lds_dwordx4 v168, vcc
	s_add_i32 m0, s50, 0x2000
	s_nop 0
	global_load_lds_dwordx4 v162, vcc
	ds_read_b128 v[180:183], v178 offset:16384
	ds_read_b128 v[184:187], v212 offset:16384
	ds_read_b128 v[188:191], v178 offset:18432
	ds_read_b128 v[192:195], v212 offset:18432
	ds_read_b128 v[196:199], v178 offset:20480
	ds_read_b128 v[200:203], v212 offset:20480
	ds_read_b128 v[204:207], v178 offset:22528
	ds_read_b128 v[208:211], v212 offset:22528
	s_waitcnt vmcnt(6)
	s_waitcnt lgkmcnt(0)
	s_barrier
	s_setprio 1
	s_waitcnt lgkmcnt(0)
	v_mfma_f32_16x16x32_bf16 v[44:47], v[130:133], v[180:183], v[44:47]
	v_mfma_f32_16x16x32_bf16 v[36:39], v[138:141], v[180:183], v[36:39]
	v_mfma_f32_16x16x32_bf16 v[28:31], v[130:133], v[188:191], v[28:31]
	v_mfma_f32_16x16x32_bf16 v[24:27], v[138:141], v[188:191], v[24:27]
	v_mfma_f32_16x16x32_bf16 v[20:23], v[130:133], v[196:199], v[20:23]
	v_mfma_f32_16x16x32_bf16 v[16:19], v[138:141], v[196:199], v[16:19]
	v_mfma_f32_16x16x32_bf16 v[12:15], v[130:133], v[204:207], v[12:15]
	v_mfma_f32_16x16x32_bf16 v[8:11], v[138:141], v[204:207], v[8:11]
	v_mfma_f32_16x16x32_bf16 v[44:47], v[134:137], v[184:187], v[44:47]
	v_mfma_f32_16x16x32_bf16 v[36:39], v[142:145], v[184:187], v[36:39]
	v_mfma_f32_16x16x32_bf16 v[28:31], v[134:137], v[192:195], v[28:31]
	v_mfma_f32_16x16x32_bf16 v[24:27], v[142:145], v[192:195], v[24:27]
	v_mfma_f32_16x16x32_bf16 v[20:23], v[134:137], v[200:203], v[20:23]
	v_mfma_f32_16x16x32_bf16 v[16:19], v[142:145], v[200:203], v[16:19]
	v_mfma_f32_16x16x32_bf16 v[12:15], v[134:137], v[208:211], v[12:15]
	v_mfma_f32_16x16x32_bf16 v[8:11], v[142:145], v[208:211], v[8:11]
	s_setprio 0
	s_setprio 1
	v_mfma_f32_16x16x32_bf16 v[4:7], v[146:149], v[180:183], v[4:7]
	v_mfma_f32_16x16x32_bf16 v[0:3], v[154:157], v[180:183], v[0:3]
	v_mfma_f32_16x16x32_bf16 v[104:107], v[146:149], v[188:191], v[104:107]
	v_mfma_f32_16x16x32_bf16 v[108:111], v[154:157], v[188:191], v[108:111]
	v_mfma_f32_16x16x32_bf16 v[112:115], v[146:149], v[196:199], v[112:115]
	v_mfma_f32_16x16x32_bf16 v[116:119], v[154:157], v[196:199], v[116:119]
	v_mfma_f32_16x16x32_bf16 v[120:123], v[146:149], v[204:207], v[120:123]
	v_mfma_f32_16x16x32_bf16 v[124:127], v[154:157], v[204:207], v[124:127]
	v_mfma_f32_16x16x32_bf16 v[4:7], v[150:153], v[184:187], v[4:7]
	v_mfma_f32_16x16x32_bf16 v[0:3], v[172:175], v[184:187], v[0:3]
	v_mfma_f32_16x16x32_bf16 v[104:107], v[150:153], v[192:195], v[104:107]
	v_mfma_f32_16x16x32_bf16 v[108:111], v[172:175], v[192:195], v[108:111]
	v_mfma_f32_16x16x32_bf16 v[112:115], v[150:153], v[200:203], v[112:115]
	v_mfma_f32_16x16x32_bf16 v[116:119], v[172:175], v[200:203], v[116:119]
	v_mfma_f32_16x16x32_bf16 v[120:123], v[150:153], v[208:211], v[120:123]
	v_mfma_f32_16x16x32_bf16 v[124:127], v[172:175], v[208:211], v[124:127]
	s_setprio 0
	s_barrier
	s_add_i32 s50, 0, 0x18000
	s_add_i32 s51, 0, 0x1c000
	v_add_u32_e32 v142, s50, v177
	v_add_u32_e32 v158, s51, v177
	ds_read_b128 v[130:133], v142
	ds_read_b128 v[134:137], v213 offset:32768
	ds_read_b128 v[138:141], v142 offset:2048
	ds_read_b128 v[142:145], v213 offset:34816
	ds_read_b128 v[146:149], v158
	ds_read_b128 v[150:153], v213 offset:49152
	ds_read_b128 v[154:157], v158 offset:2048
	ds_read_b128 v[172:175], v213 offset:51200
	s_mov_b32 m0, s29
	v_mov_b32_e32 v160, v129
	ds_read_b128 v[180:183], v178 offset:32768
	ds_read_b128 v[184:187], v212 offset:32768
	ds_read_b128 v[188:191], v178 offset:34816
	ds_read_b128 v[192:195], v212 offset:34816
	ds_read_b128 v[196:199], v178 offset:36864
	ds_read_b128 v[200:203], v212 offset:36864
	ds_read_b128 v[204:207], v178 offset:38912
	ds_read_b128 v[208:211], v212 offset:38912
	s_mov_b32 m0, s97
	s_nop 0
	global_load_lds_dwordx4 v164, s[24:25]
	s_mov_b32 m0, s28
	s_nop 0
	global_load_lds_dwordx4 v166, s[24:25]
	s_mov_b32 m0, s29
	v_mov_b32_e32 v170, v128
	global_load_lds_dwordx4 v160, s[24:25]
	s_mov_b32 m0, s30
	s_nop 0
	global_load_lds_dwordx4 v170, s[24:25]
	s_waitcnt vmcnt(8)
	s_waitcnt lgkmcnt(0)
	s_barrier
	s_setprio 1
	s_waitcnt lgkmcnt(0)
	v_mfma_f32_16x16x32_bf16 v[100:103], v[130:133], v[180:183], v[100:103]
	v_mfma_f32_16x16x32_bf16 v[96:99], v[138:141], v[180:183], v[96:99]
	v_mfma_f32_16x16x32_bf16 v[92:95], v[130:133], v[188:191], v[92:95]
	v_mfma_f32_16x16x32_bf16 v[88:91], v[138:141], v[188:191], v[88:91]
	v_mfma_f32_16x16x32_bf16 v[84:87], v[130:133], v[196:199], v[84:87]
	v_mfma_f32_16x16x32_bf16 v[80:83], v[138:141], v[196:199], v[80:83]
	v_mfma_f32_16x16x32_bf16 v[76:79], v[130:133], v[204:207], v[76:79]
	v_mfma_f32_16x16x32_bf16 v[72:75], v[138:141], v[204:207], v[72:75]
	v_mfma_f32_16x16x32_bf16 v[100:103], v[134:137], v[184:187], v[100:103]
	v_mfma_f32_16x16x32_bf16 v[96:99], v[142:145], v[184:187], v[96:99]
	v_mfma_f32_16x16x32_bf16 v[92:95], v[134:137], v[192:195], v[92:95]
	v_mfma_f32_16x16x32_bf16 v[88:91], v[142:145], v[192:195], v[88:91]
	v_mfma_f32_16x16x32_bf16 v[84:87], v[134:137], v[200:203], v[84:87]
	v_mfma_f32_16x16x32_bf16 v[80:83], v[142:145], v[200:203], v[80:83]
	v_mfma_f32_16x16x32_bf16 v[76:79], v[134:137], v[208:211], v[76:79]
	v_mfma_f32_16x16x32_bf16 v[72:75], v[142:145], v[208:211], v[72:75]
	s_setprio 0
	s_setprio 1
	v_mfma_f32_16x16x32_bf16 v[68:71], v[146:149], v[180:183], v[68:71]
	v_mfma_f32_16x16x32_bf16 v[64:67], v[154:157], v[180:183], v[64:67]
	v_mfma_f32_16x16x32_bf16 v[60:63], v[146:149], v[188:191], v[60:63]
	v_mfma_f32_16x16x32_bf16 v[56:59], v[154:157], v[188:191], v[56:59]
	v_mfma_f32_16x16x32_bf16 v[52:55], v[146:149], v[196:199], v[52:55]
	v_mfma_f32_16x16x32_bf16 v[48:51], v[154:157], v[196:199], v[48:51]
	v_mfma_f32_16x16x32_bf16 v[40:43], v[146:149], v[204:207], v[40:43]
	v_mfma_f32_16x16x32_bf16 v[32:35], v[154:157], v[204:207], v[32:35]
	v_mfma_f32_16x16x32_bf16 v[68:71], v[150:153], v[184:187], v[68:71]
	v_mfma_f32_16x16x32_bf16 v[64:67], v[172:175], v[184:187], v[64:67]
	v_mfma_f32_16x16x32_bf16 v[60:63], v[150:153], v[192:195], v[60:63]
	v_mfma_f32_16x16x32_bf16 v[56:59], v[172:175], v[192:195], v[56:59]
	v_mfma_f32_16x16x32_bf16 v[52:55], v[150:153], v[200:203], v[52:55]
	v_mfma_f32_16x16x32_bf16 v[48:51], v[172:175], v[200:203], v[48:51]
	v_mfma_f32_16x16x32_bf16 v[40:43], v[150:153], v[208:211], v[40:43]
	v_mfma_f32_16x16x32_bf16 v[32:35], v[172:175], v[208:211], v[32:35]
	s_setprio 0
	s_barrier
	v_mov_b32_e32 v169, v161
	s_add_i32 s50, s50, s61
	s_add_u32 vcc_lo, s34, s52
	s_addc_u32 vcc_hi, s35, s53
	s_mov_b32 m0, s50
	v_mov_b32_e32 v163, v161
	global_load_lds_dwordx4 v168, vcc
	s_add_i32 m0, s50, 0x2000
	v_mov_b32_e32 v165, v161
	s_add_u32 s34, s34, 0x8080
	s_addc_u32 s35, s35, 0
	s_add_i32 s50, s51, s61
	global_load_lds_dwordx4 v162, vcc
	s_mov_b32 m0, s50
	v_mov_b32_e32 v167, v161
	global_load_lds_dwordx4 v168, s[34:35]
	s_add_i32 m0, s50, 0x2000
	s_nop 0
	global_load_lds_dwordx4 v162, s[34:35]
	s_mov_b32 m0, s31
	s_add_u32 vcc_lo, s24, s52
	s_addc_u32 vcc_hi, s25, s53
	global_load_lds_dwordx4 v164, vcc
	s_mov_b32 m0, s42
	s_nop 0
	global_load_lds_dwordx4 v166, vcc
	ds_read_b128 v[180:183], v178 offset:49152
	ds_read_b128 v[184:187], v212 offset:49152
	ds_read_b128 v[188:191], v178 offset:51200
	ds_read_b128 v[192:195], v212 offset:51200
	ds_read_b128 v[196:199], v178 offset:53248
	ds_read_b128 v[200:203], v212 offset:53248
	ds_read_b128 v[204:207], v178 offset:55296
	ds_read_b128 v[208:211], v212 offset:55296
	s_waitcnt vmcnt(8)
	s_waitcnt lgkmcnt(0)
	s_barrier
	s_setprio 1
	s_waitcnt lgkmcnt(0)
	v_mfma_f32_16x16x32_bf16 v[44:47], v[130:133], v[180:183], v[44:47]
	v_mfma_f32_16x16x32_bf16 v[36:39], v[138:141], v[180:183], v[36:39]
	v_mfma_f32_16x16x32_bf16 v[28:31], v[130:133], v[188:191], v[28:31]
	v_mfma_f32_16x16x32_bf16 v[24:27], v[138:141], v[188:191], v[24:27]
	v_mfma_f32_16x16x32_bf16 v[20:23], v[130:133], v[196:199], v[20:23]
	v_mfma_f32_16x16x32_bf16 v[16:19], v[138:141], v[196:199], v[16:19]
	v_mfma_f32_16x16x32_bf16 v[12:15], v[130:133], v[204:207], v[12:15]
	v_mfma_f32_16x16x32_bf16 v[8:11], v[138:141], v[204:207], v[8:11]
	v_mfma_f32_16x16x32_bf16 v[44:47], v[134:137], v[184:187], v[44:47]
	v_mfma_f32_16x16x32_bf16 v[36:39], v[142:145], v[184:187], v[36:39]
	v_mfma_f32_16x16x32_bf16 v[28:31], v[134:137], v[192:195], v[28:31]
	v_mfma_f32_16x16x32_bf16 v[24:27], v[142:145], v[192:195], v[24:27]
	v_mfma_f32_16x16x32_bf16 v[20:23], v[134:137], v[200:203], v[20:23]
	v_mfma_f32_16x16x32_bf16 v[16:19], v[142:145], v[200:203], v[16:19]
	v_mfma_f32_16x16x32_bf16 v[12:15], v[134:137], v[208:211], v[12:15]
	v_mfma_f32_16x16x32_bf16 v[8:11], v[142:145], v[208:211], v[8:11]
	s_setprio 0
	s_setprio 1
	v_mfma_f32_16x16x32_bf16 v[4:7], v[146:149], v[180:183], v[4:7]
	v_mfma_f32_16x16x32_bf16 v[0:3], v[154:157], v[180:183], v[0:3]
	v_mfma_f32_16x16x32_bf16 v[104:107], v[146:149], v[188:191], v[104:107]
	v_mfma_f32_16x16x32_bf16 v[108:111], v[154:157], v[188:191], v[108:111]
	v_mfma_f32_16x16x32_bf16 v[112:115], v[146:149], v[196:199], v[112:115]
	v_mfma_f32_16x16x32_bf16 v[116:119], v[154:157], v[196:199], v[116:119]
	v_mfma_f32_16x16x32_bf16 v[120:123], v[146:149], v[204:207], v[120:123]
	v_mfma_f32_16x16x32_bf16 v[124:127], v[154:157], v[204:207], v[124:127]
	v_mfma_f32_16x16x32_bf16 v[4:7], v[150:153], v[184:187], v[4:7]
	v_mfma_f32_16x16x32_bf16 v[0:3], v[172:175], v[184:187], v[0:3]
	v_mfma_f32_16x16x32_bf16 v[104:107], v[150:153], v[192:195], v[104:107]
	v_mfma_f32_16x16x32_bf16 v[108:111], v[172:175], v[192:195], v[108:111]
	v_mfma_f32_16x16x32_bf16 v[112:115], v[150:153], v[200:203], v[112:115]
	v_mfma_f32_16x16x32_bf16 v[116:119], v[172:175], v[200:203], v[116:119]
	v_mfma_f32_16x16x32_bf16 v[120:123], v[150:153], v[208:211], v[120:123]
	v_mfma_f32_16x16x32_bf16 v[124:127], v[172:175], v[208:211], v[124:127]
	s_setprio 0
	s_barrier
	s_add_i32 s80, s80, 2
	s_add_u32 s6, s6, 0x100
	s_addc_u32 s7, s7, 0
	s_cmp_gt_u32 s80, 29
	s_cbranch_scc1 .LBB0_247

.LBB0_637:
	s_add_u32 s64, s6, s36
	v_add_u32_e32 v142, s53, v175
	v_add_u32_e32 v154, s54, v175
	s_addc_u32 s65, s7, s37
	ds_read_b128 v[130:133], v142
	ds_read_b128 v[138:141], v142 offset:2048
	v_xor_b32_e32 v142, 64, v142
	ds_read_b128 v[134:137], v142
	ds_read_b128 v[142:145], v142 offset:2048
	ds_read_b128 v[146:149], v154
	ds_read_b128 v[168:171], v154 offset:2048
	v_xor_b32_e32 v154, 64, v154
	ds_read_b128 v[150:153], v154
	ds_read_b128 v[178:181], v154 offset:2048
	s_add_u32 s66, s64, 0x46000100
	s_addc_u32 s67, s65, 0
	s_and_b64 s[38:39], s[40:41], exec
	s_cselect_b32 s39, s13, s67
	s_cselect_b32 s38, s12, s66
	s_add_u32 s66, s27, s36
	s_addc_u32 s67, s59, s37
	s_and_b64 s[40:41], s[40:41], exec
	s_cselect_b32 s41, s31, s67
	s_cselect_b32 s40, s30, s66
	ds_read_b128 v[182:185], v176
	ds_read_b128 v[186:189], v177
	ds_read_b128 v[190:193], v176 offset:2048
	ds_read_b128 v[194:197], v177 offset:2048
	ds_read_b128 v[198:201], v176 offset:4096
	ds_read_b128 v[202:205], v177 offset:4096
	ds_read_b128 v[206:209], v176 offset:6144
	ds_read_b128 v[210:213], v177 offset:6144
	s_add_i32 m0, s11, 0xc000
	s_add_u32 vcc_lo, s64, s20
	s_addc_u32 vcc_hi, s65, s21
	v_mov_b32_e32 v167, v157
	global_load_lds_dwordx4 v156, vcc
	s_add_i32 m0, s11, 0xe000
	s_nop 0
	global_load_lds_dwordx4 v166, vcc
	s_waitcnt vmcnt(8)
	s_waitcnt lgkmcnt(0)
	s_barrier
	s_setprio 1
	s_waitcnt lgkmcnt(0)
	v_mfma_f32_16x16x32_bf16 v[100:103], v[130:133], v[182:185], v[100:103]
	v_mfma_f32_16x16x32_bf16 v[96:99], v[138:141], v[182:185], v[96:99]
	v_mfma_f32_16x16x32_bf16 v[92:95], v[130:133], v[190:193], v[92:95]
	v_mfma_f32_16x16x32_bf16 v[88:91], v[138:141], v[190:193], v[88:91]
	v_mfma_f32_16x16x32_bf16 v[84:87], v[130:133], v[198:201], v[84:87]
	v_mfma_f32_16x16x32_bf16 v[76:79], v[138:141], v[198:201], v[76:79]
	v_mfma_f32_16x16x32_bf16 v[68:71], v[130:133], v[206:209], v[68:71]
	v_mfma_f32_16x16x32_bf16 v[60:63], v[138:141], v[206:209], v[60:63]
	v_mfma_f32_16x16x32_bf16 v[100:103], v[134:137], v[186:189], v[100:103]
	v_mfma_f32_16x16x32_bf16 v[96:99], v[142:145], v[186:189], v[96:99]
	v_mfma_f32_16x16x32_bf16 v[92:95], v[134:137], v[194:197], v[92:95]
	v_mfma_f32_16x16x32_bf16 v[88:91], v[142:145], v[194:197], v[88:91]
	v_mfma_f32_16x16x32_bf16 v[84:87], v[134:137], v[202:205], v[84:87]
	v_mfma_f32_16x16x32_bf16 v[76:79], v[142:145], v[202:205], v[76:79]
	v_mfma_f32_16x16x32_bf16 v[68:71], v[134:137], v[210:213], v[68:71]
	v_mfma_f32_16x16x32_bf16 v[60:63], v[142:145], v[210:213], v[60:63]
	s_setprio 0
	s_setprio 1
	v_mfma_f32_16x16x32_bf16 v[52:55], v[146:149], v[182:185], v[52:55]
	v_mfma_f32_16x16x32_bf16 v[44:47], v[168:171], v[182:185], v[44:47]
	v_mfma_f32_16x16x32_bf16 v[36:39], v[146:149], v[190:193], v[36:39]
	v_mfma_f32_16x16x32_bf16 v[28:31], v[168:171], v[190:193], v[28:31]
	v_mfma_f32_16x16x32_bf16 v[20:23], v[146:149], v[198:201], v[20:23]
	v_mfma_f32_16x16x32_bf16 v[12:15], v[168:171], v[198:201], v[12:15]
	v_mfma_f32_16x16x32_bf16 v[8:11], v[146:149], v[206:209], v[8:11]
	v_mfma_f32_16x16x32_bf16 v[4:7], v[168:171], v[206:209], v[4:7]
	v_mfma_f32_16x16x32_bf16 v[52:55], v[150:153], v[186:189], v[52:55]
	v_mfma_f32_16x16x32_bf16 v[44:47], v[178:181], v[186:189], v[44:47]
	v_mfma_f32_16x16x32_bf16 v[36:39], v[150:153], v[194:197], v[36:39]
	v_mfma_f32_16x16x32_bf16 v[28:31], v[178:181], v[194:197], v[28:31]
	v_mfma_f32_16x16x32_bf16 v[20:23], v[150:153], v[202:205], v[20:23]
	v_mfma_f32_16x16x32_bf16 v[12:15], v[178:181], v[202:205], v[12:15]
	v_mfma_f32_16x16x32_bf16 v[8:11], v[150:153], v[210:213], v[8:11]
	v_mfma_f32_16x16x32_bf16 v[4:7], v[178:181], v[210:213], v[4:7]
	s_setprio 0
	s_barrier
	s_add_i32 s64, s53, s42
	s_mov_b32 m0, s64
	s_nop 0
	global_load_lds_dwordx4 v164, s[40:41]
	s_add_i32 m0, s64, 0x2000
	s_add_u32 s64, s40, 0x8000
	s_addc_u32 s65, s41, 0
	s_add_i32 s66, s54, s42
	s_nop 0
	global_load_lds_dwordx4 v158, s[40:41]
	s_mov_b32 m0, s66
	s_nop 0
	global_load_lds_dwordx4 v164, s[64:65]
	s_add_i32 m0, s66, 0x2000
	s_nop 0
	global_load_lds_dwordx4 v158, s[64:65]
	ds_read_b128 v[182:185], v176 offset:16384
	ds_read_b128 v[186:189], v177 offset:16384
	ds_read_b128 v[190:193], v176 offset:18432
	ds_read_b128 v[194:197], v177 offset:18432
	ds_read_b128 v[198:201], v176 offset:20480
	ds_read_b128 v[202:205], v177 offset:20480
	ds_read_b128 v[206:209], v176 offset:22528
	ds_read_b128 v[210:213], v177 offset:22528
	s_waitcnt vmcnt(6)
	s_waitcnt lgkmcnt(0)
	s_barrier
	s_setprio 1
	s_waitcnt lgkmcnt(0)
	v_mfma_f32_16x16x32_bf16 v[80:83], v[130:133], v[182:185], v[80:83]
	v_mfma_f32_16x16x32_bf16 v[72:75], v[138:141], v[182:185], v[72:75]
	v_mfma_f32_16x16x32_bf16 v[64:67], v[130:133], v[190:193], v[64:67]
	v_mfma_f32_16x16x32_bf16 v[56:59], v[138:141], v[190:193], v[56:59]
	v_mfma_f32_16x16x32_bf16 v[48:51], v[130:133], v[198:201], v[48:51]
	v_mfma_f32_16x16x32_bf16 v[40:43], v[138:141], v[198:201], v[40:43]
	v_mfma_f32_16x16x32_bf16 v[32:35], v[130:133], v[206:209], v[32:35]
	v_mfma_f32_16x16x32_bf16 v[24:27], v[138:141], v[206:209], v[24:27]
	v_mfma_f32_16x16x32_bf16 v[80:83], v[134:137], v[186:189], v[80:83]
	v_mfma_f32_16x16x32_bf16 v[72:75], v[142:145], v[186:189], v[72:75]
	v_mfma_f32_16x16x32_bf16 v[64:67], v[134:137], v[194:197], v[64:67]
	v_mfma_f32_16x16x32_bf16 v[56:59], v[142:145], v[194:197], v[56:59]
	v_mfma_f32_16x16x32_bf16 v[48:51], v[134:137], v[202:205], v[48:51]
	v_mfma_f32_16x16x32_bf16 v[40:43], v[142:145], v[202:205], v[40:43]
	v_mfma_f32_16x16x32_bf16 v[32:35], v[134:137], v[210:213], v[32:35]
	v_mfma_f32_16x16x32_bf16 v[24:27], v[142:145], v[210:213], v[24:27]
	s_setprio 0
	s_setprio 1
	v_mfma_f32_16x16x32_bf16 v[16:19], v[146:149], v[182:185], v[16:19]
	v_mfma_f32_16x16x32_bf16 v[0:3], v[168:171], v[182:185], v[0:3]
	v_mfma_f32_16x16x32_bf16 v[104:107], v[146:149], v[190:193], v[104:107]
	v_mfma_f32_16x16x32_bf16 v[108:111], v[168:171], v[190:193], v[108:111]
	v_mfma_f32_16x16x32_bf16 v[112:115], v[146:149], v[198:201], v[112:115]
	v_mfma_f32_16x16x32_bf16 v[116:119], v[168:171], v[198:201], v[116:119]
	v_mfma_f32_16x16x32_bf16 v[120:123], v[146:149], v[206:209], v[120:123]
	v_mfma_f32_16x16x32_bf16 v[124:127], v[168:171], v[206:209], v[124:127]
	v_mfma_f32_16x16x32_bf16 v[16:19], v[150:153], v[186:189], v[16:19]
	v_mfma_f32_16x16x32_bf16 v[0:3], v[178:181], v[186:189], v[0:3]
	v_mfma_f32_16x16x32_bf16 v[104:107], v[150:153], v[194:197], v[104:107]
	v_mfma_f32_16x16x32_bf16 v[108:111], v[178:181], v[194:197], v[108:111]
	v_mfma_f32_16x16x32_bf16 v[112:115], v[150:153], v[202:205], v[112:115]
	v_mfma_f32_16x16x32_bf16 v[116:119], v[178:181], v[202:205], v[116:119]
	v_mfma_f32_16x16x32_bf16 v[120:123], v[150:153], v[210:213], v[120:123]
	v_mfma_f32_16x16x32_bf16 v[124:127], v[178:181], v[210:213], v[124:127]
	s_setprio 0
	s_barrier
	s_add_i32 s64, 0, 0x18000
	s_add_i32 s65, 0, 0x1c000
	v_add_u32_e32 v142, s64, v175
	v_add_u32_e32 v154, s65, v175
	ds_read_b128 v[130:133], v142
	ds_read_b128 v[138:141], v142 offset:2048
	v_xor_b32_e32 v142, 64, v142
	ds_read_b128 v[134:137], v142
	ds_read_b128 v[142:145], v142 offset:2048
	ds_read_b128 v[146:149], v154
	ds_read_b128 v[168:171], v154 offset:2048
	v_xor_b32_e32 v154, 64, v154
	ds_read_b128 v[150:153], v154
	ds_read_b128 v[178:181], v154 offset:2048
	s_mov_b32 m0, s45
	v_mov_b32_e32 v156, v129
	ds_read_b128 v[182:185], v176 offset:32768
	ds_read_b128 v[186:189], v177 offset:32768
	ds_read_b128 v[190:193], v176 offset:34816
	ds_read_b128 v[194:197], v177 offset:34816
	ds_read_b128 v[198:201], v176 offset:36864
	ds_read_b128 v[202:205], v177 offset:36864
	ds_read_b128 v[206:209], v176 offset:38912
	ds_read_b128 v[210:213], v177 offset:38912
	s_mov_b32 m0, s11
	s_nop 0
	global_load_lds_dwordx4 v160, s[38:39]
	s_mov_b32 m0, s44
	s_nop 0
	global_load_lds_dwordx4 v162, s[38:39]
	s_mov_b32 m0, s45
	v_mov_b32_e32 v166, v128
	global_load_lds_dwordx4 v156, s[38:39]
	s_mov_b32 m0, s46
	s_nop 0
	global_load_lds_dwordx4 v166, s[38:39]
	s_waitcnt vmcnt(8)
	s_waitcnt lgkmcnt(0)
	s_barrier
	s_setprio 1
	s_waitcnt lgkmcnt(0)
	v_mfma_f32_16x16x32_bf16 v[100:103], v[130:133], v[182:185], v[100:103]
	v_mfma_f32_16x16x32_bf16 v[96:99], v[138:141], v[182:185], v[96:99]
	v_mfma_f32_16x16x32_bf16 v[92:95], v[130:133], v[190:193], v[92:95]
	v_mfma_f32_16x16x32_bf16 v[88:91], v[138:141], v[190:193], v[88:91]
	v_mfma_f32_16x16x32_bf16 v[84:87], v[130:133], v[198:201], v[84:87]
	v_mfma_f32_16x16x32_bf16 v[76:79], v[138:141], v[198:201], v[76:79]
	v_mfma_f32_16x16x32_bf16 v[68:71], v[130:133], v[206:209], v[68:71]
	v_mfma_f32_16x16x32_bf16 v[60:63], v[138:141], v[206:209], v[60:63]
	v_mfma_f32_16x16x32_bf16 v[100:103], v[134:137], v[186:189], v[100:103]
	v_mfma_f32_16x16x32_bf16 v[96:99], v[142:145], v[186:189], v[96:99]
	v_mfma_f32_16x16x32_bf16 v[92:95], v[134:137], v[194:197], v[92:95]
	v_mfma_f32_16x16x32_bf16 v[88:91], v[142:145], v[194:197], v[88:91]
	v_mfma_f32_16x16x32_bf16 v[84:87], v[134:137], v[202:205], v[84:87]
	v_mfma_f32_16x16x32_bf16 v[76:79], v[142:145], v[202:205], v[76:79]
	v_mfma_f32_16x16x32_bf16 v[68:71], v[134:137], v[210:213], v[68:71]
	v_mfma_f32_16x16x32_bf16 v[60:63], v[142:145], v[210:213], v[60:63]
	s_setprio 0
	s_setprio 1
	v_mfma_f32_16x16x32_bf16 v[52:55], v[146:149], v[182:185], v[52:55]
	v_mfma_f32_16x16x32_bf16 v[44:47], v[168:171], v[182:185], v[44:47]
	v_mfma_f32_16x16x32_bf16 v[36:39], v[146:149], v[190:193], v[36:39]
	v_mfma_f32_16x16x32_bf16 v[28:31], v[168:171], v[190:193], v[28:31]
	v_mfma_f32_16x16x32_bf16 v[20:23], v[146:149], v[198:201], v[20:23]
	v_mfma_f32_16x16x32_bf16 v[12:15], v[168:171], v[198:201], v[12:15]
	v_mfma_f32_16x16x32_bf16 v[8:11], v[146:149], v[206:209], v[8:11]
	v_mfma_f32_16x16x32_bf16 v[4:7], v[168:171], v[206:209], v[4:7]
	v_mfma_f32_16x16x32_bf16 v[52:55], v[150:153], v[186:189], v[52:55]
	v_mfma_f32_16x16x32_bf16 v[44:47], v[178:181], v[186:189], v[44:47]
	v_mfma_f32_16x16x32_bf16 v[36:39], v[150:153], v[194:197], v[36:39]
	v_mfma_f32_16x16x32_bf16 v[28:31], v[178:181], v[194:197], v[28:31]
	v_mfma_f32_16x16x32_bf16 v[20:23], v[150:153], v[202:205], v[20:23]
	v_mfma_f32_16x16x32_bf16 v[12:15], v[178:181], v[202:205], v[12:15]
	v_mfma_f32_16x16x32_bf16 v[8:11], v[150:153], v[210:213], v[8:11]
	v_mfma_f32_16x16x32_bf16 v[4:7], v[178:181], v[210:213], v[4:7]
	s_setprio 0
	s_barrier
	v_mov_b32_e32 v165, v157
	s_add_i32 s64, s64, s42
	s_add_u32 vcc_lo, s40, s18
	s_addc_u32 vcc_hi, s41, s19
	s_mov_b32 m0, s64
	v_mov_b32_e32 v159, v157
	global_load_lds_dwordx4 v164, vcc
	s_add_i32 m0, s64, 0x2000
	v_mov_b32_e32 v161, v157
	s_add_u32 s40, s40, 0x8080
	s_addc_u32 s41, s41, 0
	s_add_i32 s64, s65, s42
	global_load_lds_dwordx4 v158, vcc
	s_mov_b32 m0, s64
	v_mov_b32_e32 v163, v157
	global_load_lds_dwordx4 v164, s[40:41]
	s_add_i32 m0, s64, 0x2000
	s_nop 0
	global_load_lds_dwordx4 v158, s[40:41]
	s_mov_b32 m0, s49
	s_add_u32 vcc_lo, s38, s18
	s_addc_u32 vcc_hi, s39, s19
	global_load_lds_dwordx4 v160, vcc
	s_mov_b32 m0, s50
	s_nop 0
	global_load_lds_dwordx4 v162, vcc
	ds_read_b128 v[182:185], v176 offset:49152
	ds_read_b128 v[186:189], v177 offset:49152
	ds_read_b128 v[190:193], v176 offset:51200
	ds_read_b128 v[194:197], v177 offset:51200
	ds_read_b128 v[198:201], v176 offset:53248
	ds_read_b128 v[202:205], v177 offset:53248
	ds_read_b128 v[206:209], v176 offset:55296
	ds_read_b128 v[210:213], v177 offset:55296
	s_waitcnt vmcnt(8)
	s_waitcnt lgkmcnt(0)
	s_barrier
	s_setprio 1
	s_waitcnt lgkmcnt(0)
	v_mfma_f32_16x16x32_bf16 v[80:83], v[130:133], v[182:185], v[80:83]
	v_mfma_f32_16x16x32_bf16 v[72:75], v[138:141], v[182:185], v[72:75]
	v_mfma_f32_16x16x32_bf16 v[64:67], v[130:133], v[190:193], v[64:67]
	v_mfma_f32_16x16x32_bf16 v[56:59], v[138:141], v[190:193], v[56:59]
	v_mfma_f32_16x16x32_bf16 v[48:51], v[130:133], v[198:201], v[48:51]
	v_mfma_f32_16x16x32_bf16 v[40:43], v[138:141], v[198:201], v[40:43]
	v_mfma_f32_16x16x32_bf16 v[32:35], v[130:133], v[206:209], v[32:35]
	v_mfma_f32_16x16x32_bf16 v[24:27], v[138:141], v[206:209], v[24:27]
	v_mfma_f32_16x16x32_bf16 v[80:83], v[134:137], v[186:189], v[80:83]
	v_mfma_f32_16x16x32_bf16 v[72:75], v[142:145], v[186:189], v[72:75]
	v_mfma_f32_16x16x32_bf16 v[64:67], v[134:137], v[194:197], v[64:67]
	v_mfma_f32_16x16x32_bf16 v[56:59], v[142:145], v[194:197], v[56:59]
	v_mfma_f32_16x16x32_bf16 v[48:51], v[134:137], v[202:205], v[48:51]
	v_mfma_f32_16x16x32_bf16 v[40:43], v[142:145], v[202:205], v[40:43]
	v_mfma_f32_16x16x32_bf16 v[32:35], v[134:137], v[210:213], v[32:35]
	v_mfma_f32_16x16x32_bf16 v[24:27], v[142:145], v[210:213], v[24:27]
	s_setprio 0
	s_setprio 1
	v_mfma_f32_16x16x32_bf16 v[16:19], v[146:149], v[182:185], v[16:19]
	v_mfma_f32_16x16x32_bf16 v[0:3], v[168:171], v[182:185], v[0:3]
	v_mfma_f32_16x16x32_bf16 v[104:107], v[146:149], v[190:193], v[104:107]
	v_mfma_f32_16x16x32_bf16 v[108:111], v[168:171], v[190:193], v[108:111]
	v_mfma_f32_16x16x32_bf16 v[112:115], v[146:149], v[198:201], v[112:115]
	v_mfma_f32_16x16x32_bf16 v[116:119], v[168:171], v[198:201], v[116:119]
	v_mfma_f32_16x16x32_bf16 v[120:123], v[146:149], v[206:209], v[120:123]
	v_mfma_f32_16x16x32_bf16 v[124:127], v[168:171], v[206:209], v[124:127]
	v_mfma_f32_16x16x32_bf16 v[16:19], v[150:153], v[186:189], v[16:19]
	v_mfma_f32_16x16x32_bf16 v[0:3], v[178:181], v[186:189], v[0:3]
	v_mfma_f32_16x16x32_bf16 v[104:107], v[150:153], v[194:197], v[104:107]
	v_mfma_f32_16x16x32_bf16 v[108:111], v[178:181], v[194:197], v[108:111]
	v_mfma_f32_16x16x32_bf16 v[112:115], v[150:153], v[202:205], v[112:115]
	v_mfma_f32_16x16x32_bf16 v[116:119], v[178:181], v[202:205], v[116:119]
	v_mfma_f32_16x16x32_bf16 v[120:123], v[150:153], v[210:213], v[120:123]
	v_mfma_f32_16x16x32_bf16 v[124:127], v[178:181], v[210:213], v[124:127]
	s_setprio 0
	s_barrier
	s_add_i32 s63, s63, 2
	s_add_u32 s36, s36, 0x100
	s_addc_u32 s37, s37, 0
	s_cmp_gt_u32 s63, 29
	s_cbranch_scc1 .LBB0_642

.LBB0_910:
	s_add_u32 s25, s36, 0x100
	s_addc_u32 s27, s37, 0
	s_lshl_b32 s7, s55, 10
	s_add_i32 s7, s7, 0x24000
	s_mov_b32 s42, -2
	s_mov_b64 s[36:37], 0
	s_cmp_eq_u32 s42, 12
	s_cselect_b64 s[40:41], -1, 0
	s_and_b64 s[38:39], s[34:35], s[40:41]
	s_andn2_b64 vcc, exec, s[38:39]
	v_mov_b32_e32 v128, v186
	v_mov_b32_e32 v129, v176
	s_add_u32 s76, s10, s36
	s_addc_u32 s77, s11, s37
	ds_read_b128 v[130:133], v220
	ds_read_b128 v[138:141], v220 offset:2048
	ds_read_b128 v[134:137], v221
	ds_read_b128 v[142:145], v221 offset:2048
	ds_read_b128 v[146:149], v222
	ds_read_b128 v[154:157], v222 offset:2048
	ds_read_b128 v[150:153], v223
	ds_read_b128 v[158:161], v223 offset:2048
	s_add_u32 s43, s76, 0x36000100
	s_addc_u32 s75, s77, 0
	s_and_b64 s[38:39], s[40:41], exec
	s_cselect_b32 s39, s13, s75
	s_cselect_b32 s38, s12, s43
	s_add_u32 s43, s25, s36
	s_addc_u32 s75, s27, s37
	s_and_b64 s[40:41], s[40:41], exec
	s_cselect_b32 s41, s31, s75
	s_cselect_b32 s40, s30, s43
	ds_read_b128 v[162:165], v227
	ds_read_b128 v[232:235], v227 offset:2048
	ds_read_b128 v[166:169], v228
	ds_read_b128 v[236:239], v228 offset:2048
	ds_read_b128 v[240:243], v227 offset:4096
	ds_read_b128 v[196:199], v227 offset:6144
	ds_read_b128 v[244:247], v228 offset:4096
	ds_read_b128 v[200:203], v228 offset:6144
	s_add_i32 m0, s50, 0xc000
	s_add_u32 vcc_lo, s76, s16
	s_addc_u32 vcc_hi, s77, s17
	global_load_lds_dwordx4 v176, vcc
	s_add_i32 m0, s50, 0xe000
	s_nop 0
	global_load_lds_dwordx4 v186, vcc
	s_waitcnt vmcnt(8)
	s_waitcnt lgkmcnt(0)
	s_barrier
	s_setprio 1
	s_waitcnt lgkmcnt(0)
	v_mfma_f32_16x16x128_f8f6f4 v[100:103], v[130:137], v[162:169], 0
	v_mfma_f32_16x16x128_f8f6f4 v[96:99], v[138:145], v[162:169], 0
	v_mfma_f32_16x16x128_f8f6f4 v[92:95], v[130:137], v[232:239], 0
	v_mfma_f32_16x16x128_f8f6f4 v[88:91], v[138:145], v[232:239], 0
	v_mfma_f32_16x16x128_f8f6f4 v[84:87], v[130:137], v[240:247], 0
	v_mfma_f32_16x16x128_f8f6f4 v[80:83], v[138:145], v[240:247], 0
	v_mfma_f32_16x16x128_f8f6f4 v[170:173], v[130:137], v[196:203], 0
	v_mfma_f32_16x16x128_f8f6f4 v[188:191], v[138:145], v[196:203], 0
	s_setprio 0
	s_setprio 1
	v_mfma_f32_16x16x128_f8f6f4 v[40:43], v[146:153], v[196:203], 0
	v_mfma_f32_16x16x128_f8f6f4 v[32:35], v[154:161], v[196:203], 0
	v_mfma_f32_16x16x128_f8f6f4 v[248:251], v[146:153], v[162:169], 0
	v_mfma_f32_16x16x128_f8f6f4 v[204:207], v[154:161], v[162:169], 0
	v_mfma_f32_16x16x128_f8f6f4 v[208:211], v[146:153], v[232:239], 0
	v_mfma_f32_16x16x128_f8f6f4 v[212:215], v[154:161], v[232:239], 0
	v_mfma_f32_16x16x128_f8f6f4 v[216:219], v[146:153], v[240:247], 0
	v_mfma_f32_16x16x128_f8f6f4 v[240:243], v[154:161], v[240:247], 0
	s_setprio 0
	s_barrier
	s_add_i32 s43, s67, s5
	s_mov_b32 m0, s43
	s_nop 2
	s_nop 0
	global_load_lds_dwordx4 v184, s[40:41]
	s_add_i32 m0, s43, 0x2000
	s_add_u32 s76, s40, 0x4000
	s_addc_u32 s77, s41, 0
	s_add_i32 s43, s68, s5
	s_nop 0
	global_load_lds_dwordx4 v178, s[40:41]
	s_mov_b32 m0, s43
	s_nop 0
	global_load_lds_dwordx4 v184, s[76:77]
	s_add_i32 m0, s43, 0x2000
	s_nop 0
	global_load_lds_dwordx4 v178, s[76:77]
	ds_read_b128 v[48:51], v227 offset:16384
	ds_read_b128 v[56:59], v227 offset:18432
	ds_read_b128 v[52:55], v228 offset:16384
	ds_read_b128 v[60:63], v228 offset:18432
	ds_read_b128 v[64:67], v227 offset:20480
	ds_read_b128 v[72:75], v227 offset:22528
	ds_read_b128 v[68:71], v228 offset:20480
	ds_read_b128 v[76:79], v228 offset:22528
	s_waitcnt vmcnt(6)
	s_waitcnt lgkmcnt(0)
	s_barrier
	s_setprio 1
	s_waitcnt lgkmcnt(0)
	v_mfma_f32_16x16x128_f8f6f4 v[44:47], v[130:137], v[48:55], 0
	v_mfma_f32_16x16x128_f8f6f4 v[36:39], v[138:145], v[48:55], 0
	v_mfma_f32_16x16x128_f8f6f4 v[28:31], v[130:137], v[56:63], 0
	v_mfma_f32_16x16x128_f8f6f4 v[24:27], v[138:145], v[56:63], 0
	v_mfma_f32_16x16x128_f8f6f4 v[20:23], v[130:137], v[64:71], 0
	v_mfma_f32_16x16x128_f8f6f4 v[16:19], v[138:145], v[64:71], 0
	v_mfma_f32_16x16x128_f8f6f4 v[12:15], v[130:137], v[72:79], 0
	v_mfma_f32_16x16x128_f8f6f4 v[8:11], v[138:145], v[72:79], 0
	s_setprio 0
	s_setprio 1
	v_mfma_f32_16x16x128_f8f6f4 v[4:7], v[146:153], v[48:55], 0
	v_mfma_f32_16x16x128_f8f6f4 v[0:3], v[154:161], v[48:55], 0
	v_mfma_f32_16x16x128_f8f6f4 v[104:107], v[146:153], v[56:63], 0
	v_mfma_f32_16x16x128_f8f6f4 v[108:111], v[154:161], v[56:63], 0
	v_mfma_f32_16x16x128_f8f6f4 v[112:115], v[146:153], v[64:71], 0
	v_mfma_f32_16x16x128_f8f6f4 v[116:119], v[154:161], v[64:71], 0
	v_mfma_f32_16x16x128_f8f6f4 v[120:123], v[146:153], v[72:79], 0
	v_mfma_f32_16x16x128_f8f6f4 v[124:127], v[154:161], v[72:79], 0
	s_setprio 0
	s_barrier
	s_add_i32 s43, 0, 0x18000
	s_add_i32 s75, 0, 0x1c000
	ds_read_b128 v[130:133], v224
	ds_read_b128 v[138:141], v224 offset:2048
	ds_read_b128 v[134:137], v225
	ds_read_b128 v[142:145], v225 offset:2048
	ds_read_b128 v[146:149], v226
	ds_read_b128 v[154:157], v226 offset:2048
	ds_read_b128 v[150:153], v229
	ds_read_b128 v[158:161], v229 offset:2048
	s_mov_b32 m0, s52
	v_mov_b32_e32 v176, v129
	ds_read_b128 v[48:51], v227 offset:32768
	ds_read_b128 v[162:165], v227 offset:34816
	ds_read_b128 v[52:55], v228 offset:32768
	ds_read_b128 v[166:169], v228 offset:34816
	ds_read_b128 v[196:199], v227 offset:36864
	ds_read_b128 v[232:235], v227 offset:38912
	ds_read_b128 v[200:203], v228 offset:36864
	ds_read_b128 v[236:239], v228 offset:38912
	s_mov_b32 m0, s50
	s_nop 0
	global_load_lds_dwordx4 v180, s[38:39]
	s_mov_b32 m0, s51
	s_nop 0
	global_load_lds_dwordx4 v182, s[38:39]
	s_mov_b32 m0, s52
	v_mov_b32_e32 v186, v128
	global_load_lds_dwordx4 v176, s[38:39]
	s_mov_b32 m0, s53
	s_nop 0
	global_load_lds_dwordx4 v186, s[38:39]
	s_waitcnt vmcnt(8)
	s_waitcnt lgkmcnt(0)
	s_barrier
	s_setprio 1
	s_waitcnt lgkmcnt(0)
	v_mfma_f32_16x16x128_f8f6f4 v[100:103], v[130:137], v[48:55], v[100:103]
	v_mfma_f32_16x16x128_f8f6f4 v[96:99], v[138:145], v[48:55], v[96:99]
	v_mfma_f32_16x16x128_f8f6f4 v[92:95], v[130:137], v[162:169], v[92:95]
	v_mfma_f32_16x16x128_f8f6f4 v[88:91], v[138:145], v[162:169], v[88:91]
	v_mfma_f32_16x16x128_f8f6f4 v[84:87], v[130:137], v[196:203], v[84:87]
	v_mfma_f32_16x16x128_f8f6f4 v[80:83], v[138:145], v[196:203], v[80:83]
	v_mfma_f32_16x16x128_f8f6f4 v[76:79], v[130:137], v[232:239], v[170:173]
	v_mfma_f32_16x16x128_f8f6f4 v[72:75], v[138:145], v[232:239], v[188:191]
	s_setprio 0
	s_setprio 1
	v_mfma_f32_16x16x128_f8f6f4 v[68:71], v[146:153], v[48:55], v[248:251]
	v_mfma_f32_16x16x128_f8f6f4 v[64:67], v[154:161], v[48:55], v[204:207]
	v_mfma_f32_16x16x128_f8f6f4 v[60:63], v[146:153], v[162:169], v[208:211]
	v_mfma_f32_16x16x128_f8f6f4 v[56:59], v[154:161], v[162:169], v[212:215]
	v_mfma_f32_16x16x128_f8f6f4 v[52:55], v[146:153], v[196:203], v[216:219]
	v_mfma_f32_16x16x128_f8f6f4 v[48:51], v[154:161], v[196:203], v[240:243]
	v_mfma_f32_16x16x128_f8f6f4 v[40:43], v[146:153], v[232:239], v[40:43]
	v_mfma_f32_16x16x128_f8f6f4 v[32:35], v[154:161], v[232:239], v[32:35]
	s_setprio 0
	s_barrier
	s_add_i32 s43, s43, s5
	s_add_u32 vcc_lo, s40, s14
	s_addc_u32 vcc_hi, s41, s15
	s_mov_b32 m0, s43
	global_load_lds_dwordx4 v184, vcc
	s_add_i32 m0, s43, 0x2000
	s_add_u32 s40, s40, 0x4080
	s_addc_u32 s41, s41, 0
	s_add_i32 s43, s75, s5
	global_load_lds_dwordx4 v178, vcc
	s_mov_b32 m0, s43
	global_load_lds_dwordx4 v184, s[40:41]
	s_add_i32 m0, s43, 0x2000
	s_nop 0
	global_load_lds_dwordx4 v178, s[40:41]
	s_mov_b32 m0, s62
	s_add_u32 vcc_lo, s38, s14
	s_addc_u32 vcc_hi, s39, s15
	global_load_lds_dwordx4 v180, vcc
	s_mov_b32 m0, s63
	s_nop 0
	global_load_lds_dwordx4 v182, vcc
	ds_read_b128 v[162:165], v227 offset:49152
	ds_read_b128 v[196:199], v227 offset:51200
	ds_read_b128 v[166:169], v228 offset:49152
	ds_read_b128 v[200:203], v228 offset:51200
	ds_read_b128 v[232:235], v227 offset:53248
	ds_read_b128 v[240:243], v227 offset:55296
	ds_read_b128 v[236:239], v228 offset:53248
	ds_read_b128 v[244:247], v228 offset:55296
	s_waitcnt vmcnt(8)
	s_waitcnt lgkmcnt(0)
	s_barrier
	s_setprio 1
	s_waitcnt lgkmcnt(0)
	v_mfma_f32_16x16x128_f8f6f4 v[44:47], v[130:137], v[162:169], v[44:47]
	v_mfma_f32_16x16x128_f8f6f4 v[36:39], v[138:145], v[162:169], v[36:39]
	v_mfma_f32_16x16x128_f8f6f4 v[28:31], v[130:137], v[196:203], v[28:31]
	v_mfma_f32_16x16x128_f8f6f4 v[24:27], v[138:145], v[196:203], v[24:27]
	v_mfma_f32_16x16x128_f8f6f4 v[20:23], v[130:137], v[232:239], v[20:23]
	v_mfma_f32_16x16x128_f8f6f4 v[16:19], v[138:145], v[232:239], v[16:19]
	v_mfma_f32_16x16x128_f8f6f4 v[12:15], v[130:137], v[240:247], v[12:15]
	v_mfma_f32_16x16x128_f8f6f4 v[8:11], v[138:145], v[240:247], v[8:11]
	s_setprio 0
	s_setprio 1
	v_mfma_f32_16x16x128_f8f6f4 v[4:7], v[146:153], v[162:169], v[4:7]
	v_mfma_f32_16x16x128_f8f6f4 v[0:3], v[154:161], v[162:169], v[0:3]
	v_mfma_f32_16x16x128_f8f6f4 v[104:107], v[146:153], v[196:203], v[104:107]
	v_mfma_f32_16x16x128_f8f6f4 v[108:111], v[154:161], v[196:203], v[108:111]
	v_mfma_f32_16x16x128_f8f6f4 v[112:115], v[146:153], v[232:239], v[112:115]
	v_mfma_f32_16x16x128_f8f6f4 v[116:119], v[154:161], v[232:239], v[116:119]
	v_mfma_f32_16x16x128_f8f6f4 v[120:123], v[146:153], v[240:247], v[120:123]
	v_mfma_f32_16x16x128_f8f6f4 v[124:127], v[154:161], v[240:247], v[124:127]
	s_setprio 0
	s_barrier
	s_add_i32 s42, s42, 2
	s_add_u32 s36, s36, 0x100
	s_addc_u32 s37, s37, 0
	s_branch .LBB0_912
.LBB0_911:
	s_add_u32 s76, s10, s36
	s_addc_u32 s77, s11, s37
	ds_read_b128 v[130:133], v220
	ds_read_b128 v[138:141], v220 offset:2048
	ds_read_b128 v[134:137], v221
	ds_read_b128 v[142:145], v221 offset:2048
	ds_read_b128 v[146:149], v222
	ds_read_b128 v[154:157], v222 offset:2048
	ds_read_b128 v[150:153], v223
	ds_read_b128 v[158:161], v223 offset:2048
	s_add_u32 s43, s76, 0x36000100
	s_addc_u32 s75, s77, 0
	s_and_b64 s[38:39], s[40:41], exec
	s_cselect_b32 s39, s13, s75
	s_cselect_b32 s38, s12, s43
	s_add_u32 s43, s25, s36
	s_addc_u32 s75, s27, s37
	s_and_b64 s[40:41], s[40:41], exec
	s_cselect_b32 s41, s31, s75
	s_cselect_b32 s40, s30, s43
	ds_read_b128 v[162:165], v227
	ds_read_b128 v[232:235], v227 offset:2048
	ds_read_b128 v[166:169], v228
	ds_read_b128 v[236:239], v228 offset:2048
	ds_read_b128 v[240:243], v227 offset:4096
	ds_read_b128 v[196:199], v227 offset:6144
	ds_read_b128 v[244:247], v228 offset:4096
	ds_read_b128 v[200:203], v228 offset:6144
	s_add_i32 m0, s50, 0xc000
	s_add_u32 vcc_lo, s76, s16
	s_addc_u32 vcc_hi, s77, s17
	global_load_lds_dwordx4 v176, vcc
	s_add_i32 m0, s50, 0xe000
	s_nop 0
	global_load_lds_dwordx4 v186, vcc
	s_waitcnt vmcnt(8)
	s_waitcnt lgkmcnt(0)
	s_barrier
	s_setprio 1
	s_waitcnt lgkmcnt(0)
	v_mfma_f32_16x16x128_f8f6f4 v[100:103], v[130:137], v[162:169], v[100:103]
	v_mfma_f32_16x16x128_f8f6f4 v[96:99], v[138:145], v[162:169], v[96:99]
	v_mfma_f32_16x16x128_f8f6f4 v[92:95], v[130:137], v[232:239], v[92:95]
	v_mfma_f32_16x16x128_f8f6f4 v[88:91], v[138:145], v[232:239], v[88:91]
	v_mfma_f32_16x16x128_f8f6f4 v[84:87], v[130:137], v[240:247], v[84:87]
	v_mfma_f32_16x16x128_f8f6f4 v[80:83], v[138:145], v[240:247], v[80:83]
	v_mfma_f32_16x16x128_f8f6f4 v[170:173], v[130:137], v[196:203], v[76:79]
	v_mfma_f32_16x16x128_f8f6f4 v[188:191], v[138:145], v[196:203], v[72:75]
	s_setprio 0
	s_setprio 1
	v_mfma_f32_16x16x128_f8f6f4 v[40:43], v[146:153], v[196:203], v[40:43]
	v_mfma_f32_16x16x128_f8f6f4 v[32:35], v[154:161], v[196:203], v[32:35]
	v_mfma_f32_16x16x128_f8f6f4 v[248:251], v[146:153], v[162:169], v[68:71]
	v_mfma_f32_16x16x128_f8f6f4 v[204:207], v[154:161], v[162:169], v[64:67]
	v_mfma_f32_16x16x128_f8f6f4 v[208:211], v[146:153], v[232:239], v[60:63]
	v_mfma_f32_16x16x128_f8f6f4 v[212:215], v[154:161], v[232:239], v[56:59]
	v_mfma_f32_16x16x128_f8f6f4 v[216:219], v[146:153], v[240:247], v[52:55]
	v_mfma_f32_16x16x128_f8f6f4 v[240:243], v[154:161], v[240:247], v[48:51]
	s_setprio 0
	s_barrier
	s_add_i32 s43, s67, s5
	s_mov_b32 m0, s43
	s_nop 2
	s_nop 0
	global_load_lds_dwordx4 v184, s[40:41]
	s_add_i32 m0, s43, 0x2000
	s_add_u32 s76, s40, 0x4000
	s_addc_u32 s77, s41, 0
	s_add_i32 s43, s68, s5
	s_nop 0
	global_load_lds_dwordx4 v178, s[40:41]
	s_mov_b32 m0, s43
	s_nop 0
	global_load_lds_dwordx4 v184, s[76:77]
	s_add_i32 m0, s43, 0x2000
	s_nop 0
	global_load_lds_dwordx4 v178, s[76:77]
	ds_read_b128 v[48:51], v227 offset:16384
	ds_read_b128 v[56:59], v227 offset:18432
	ds_read_b128 v[52:55], v228 offset:16384
	ds_read_b128 v[60:63], v228 offset:18432
	ds_read_b128 v[64:67], v227 offset:20480
	ds_read_b128 v[72:75], v227 offset:22528
	ds_read_b128 v[68:71], v228 offset:20480
	ds_read_b128 v[76:79], v228 offset:22528
	s_waitcnt vmcnt(6)
	s_waitcnt lgkmcnt(0)
	s_barrier
	s_setprio 1
	s_waitcnt lgkmcnt(0)
	v_mfma_f32_16x16x128_f8f6f4 v[44:47], v[130:137], v[48:55], v[44:47]
	v_mfma_f32_16x16x128_f8f6f4 v[36:39], v[138:145], v[48:55], v[36:39]
	v_mfma_f32_16x16x128_f8f6f4 v[28:31], v[130:137], v[56:63], v[28:31]
	v_mfma_f32_16x16x128_f8f6f4 v[24:27], v[138:145], v[56:63], v[24:27]
	v_mfma_f32_16x16x128_f8f6f4 v[20:23], v[130:137], v[64:71], v[20:23]
	v_mfma_f32_16x16x128_f8f6f4 v[16:19], v[138:145], v[64:71], v[16:19]
	v_mfma_f32_16x16x128_f8f6f4 v[12:15], v[130:137], v[72:79], v[12:15]
	v_mfma_f32_16x16x128_f8f6f4 v[8:11], v[138:145], v[72:79], v[8:11]
	s_setprio 0
	s_setprio 1
	v_mfma_f32_16x16x128_f8f6f4 v[4:7], v[146:153], v[48:55], v[4:7]
	v_mfma_f32_16x16x128_f8f6f4 v[0:3], v[154:161], v[48:55], v[0:3]
	v_mfma_f32_16x16x128_f8f6f4 v[104:107], v[146:153], v[56:63], v[104:107]
	v_mfma_f32_16x16x128_f8f6f4 v[108:111], v[154:161], v[56:63], v[108:111]
	v_mfma_f32_16x16x128_f8f6f4 v[112:115], v[146:153], v[64:71], v[112:115]
	v_mfma_f32_16x16x128_f8f6f4 v[116:119], v[154:161], v[64:71], v[116:119]
	v_mfma_f32_16x16x128_f8f6f4 v[120:123], v[146:153], v[72:79], v[120:123]
	v_mfma_f32_16x16x128_f8f6f4 v[124:127], v[154:161], v[72:79], v[124:127]
	s_setprio 0
	s_barrier
	s_add_i32 s43, 0, 0x18000
	s_add_i32 s75, 0, 0x1c000
	ds_read_b128 v[130:133], v224
	ds_read_b128 v[138:141], v224 offset:2048
	ds_read_b128 v[134:137], v225
	ds_read_b128 v[142:145], v225 offset:2048
	ds_read_b128 v[146:149], v226
	ds_read_b128 v[154:157], v226 offset:2048
	ds_read_b128 v[150:153], v229
	ds_read_b128 v[158:161], v229 offset:2048
	s_mov_b32 m0, s52
	v_mov_b32_e32 v176, v129
	ds_read_b128 v[48:51], v227 offset:32768
	ds_read_b128 v[162:165], v227 offset:34816
	ds_read_b128 v[52:55], v228 offset:32768
	ds_read_b128 v[166:169], v228 offset:34816
	ds_read_b128 v[196:199], v227 offset:36864
	ds_read_b128 v[232:235], v227 offset:38912
	ds_read_b128 v[200:203], v228 offset:36864
	ds_read_b128 v[236:239], v228 offset:38912
	s_mov_b32 m0, s50
	s_nop 0
	global_load_lds_dwordx4 v180, s[38:39]
	s_mov_b32 m0, s51
	s_nop 0
	global_load_lds_dwordx4 v182, s[38:39]
	s_mov_b32 m0, s52
	v_mov_b32_e32 v186, v128
	global_load_lds_dwordx4 v176, s[38:39]
	s_mov_b32 m0, s53
	s_nop 0
	global_load_lds_dwordx4 v186, s[38:39]
	s_waitcnt vmcnt(8)
	s_waitcnt lgkmcnt(0)
	s_barrier
	s_setprio 1
	s_waitcnt lgkmcnt(0)
	v_mfma_f32_16x16x128_f8f6f4 v[100:103], v[130:137], v[48:55], v[100:103]
	v_mfma_f32_16x16x128_f8f6f4 v[96:99], v[138:145], v[48:55], v[96:99]
	v_mfma_f32_16x16x128_f8f6f4 v[92:95], v[130:137], v[162:169], v[92:95]
	v_mfma_f32_16x16x128_f8f6f4 v[88:91], v[138:145], v[162:169], v[88:91]
	v_mfma_f32_16x16x128_f8f6f4 v[84:87], v[130:137], v[196:203], v[84:87]
	v_mfma_f32_16x16x128_f8f6f4 v[80:83], v[138:145], v[196:203], v[80:83]
	v_mfma_f32_16x16x128_f8f6f4 v[76:79], v[130:137], v[232:239], v[170:173]
	v_mfma_f32_16x16x128_f8f6f4 v[72:75], v[138:145], v[232:239], v[188:191]
	s_setprio 0
	s_setprio 1
	v_mfma_f32_16x16x128_f8f6f4 v[68:71], v[146:153], v[48:55], v[248:251]
	v_mfma_f32_16x16x128_f8f6f4 v[64:67], v[154:161], v[48:55], v[204:207]
	v_mfma_f32_16x16x128_f8f6f4 v[60:63], v[146:153], v[162:169], v[208:211]
	v_mfma_f32_16x16x128_f8f6f4 v[56:59], v[154:161], v[162:169], v[212:215]
	v_mfma_f32_16x16x128_f8f6f4 v[52:55], v[146:153], v[196:203], v[216:219]
	v_mfma_f32_16x16x128_f8f6f4 v[48:51], v[154:161], v[196:203], v[240:243]
	v_mfma_f32_16x16x128_f8f6f4 v[40:43], v[146:153], v[232:239], v[40:43]
	v_mfma_f32_16x16x128_f8f6f4 v[32:35], v[154:161], v[232:239], v[32:35]
	s_setprio 0
	s_barrier
	s_add_i32 s43, s43, s5
	s_add_u32 vcc_lo, s40, s14
	s_addc_u32 vcc_hi, s41, s15
	s_mov_b32 m0, s43
	global_load_lds_dwordx4 v184, vcc
	s_add_i32 m0, s43, 0x2000
	s_add_u32 s40, s40, 0x4080
	s_addc_u32 s41, s41, 0
	s_add_i32 s43, s75, s5
	global_load_lds_dwordx4 v178, vcc
	s_mov_b32 m0, s43
	global_load_lds_dwordx4 v184, s[40:41]
	s_add_i32 m0, s43, 0x2000
	s_nop 0
	global_load_lds_dwordx4 v178, s[40:41]
	s_mov_b32 m0, s62
	s_add_u32 vcc_lo, s38, s14
	s_addc_u32 vcc_hi, s39, s15
	global_load_lds_dwordx4 v180, vcc
	s_mov_b32 m0, s63
	s_nop 0
	global_load_lds_dwordx4 v182, vcc
	ds_read_b128 v[162:165], v227 offset:49152
	ds_read_b128 v[196:199], v227 offset:51200
	ds_read_b128 v[166:169], v228 offset:49152
	ds_read_b128 v[200:203], v228 offset:51200
	ds_read_b128 v[232:235], v227 offset:53248
	ds_read_b128 v[240:243], v227 offset:55296
	ds_read_b128 v[236:239], v228 offset:53248
	ds_read_b128 v[244:247], v228 offset:55296
	s_waitcnt vmcnt(8)
	s_waitcnt lgkmcnt(0)
	s_barrier
	s_setprio 1
	s_waitcnt lgkmcnt(0)
	v_mfma_f32_16x16x128_f8f6f4 v[44:47], v[130:137], v[162:169], v[44:47]
	v_mfma_f32_16x16x128_f8f6f4 v[36:39], v[138:145], v[162:169], v[36:39]
	v_mfma_f32_16x16x128_f8f6f4 v[28:31], v[130:137], v[196:203], v[28:31]
	v_mfma_f32_16x16x128_f8f6f4 v[24:27], v[138:145], v[196:203], v[24:27]
	v_mfma_f32_16x16x128_f8f6f4 v[20:23], v[130:137], v[232:239], v[20:23]
	v_mfma_f32_16x16x128_f8f6f4 v[16:19], v[138:145], v[232:239], v[16:19]
	v_mfma_f32_16x16x128_f8f6f4 v[12:15], v[130:137], v[240:247], v[12:15]
	v_mfma_f32_16x16x128_f8f6f4 v[8:11], v[138:145], v[240:247], v[8:11]
	s_setprio 0
	s_setprio 1
	v_mfma_f32_16x16x128_f8f6f4 v[4:7], v[146:153], v[162:169], v[4:7]
	v_mfma_f32_16x16x128_f8f6f4 v[0:3], v[154:161], v[162:169], v[0:3]
	v_mfma_f32_16x16x128_f8f6f4 v[104:107], v[146:153], v[196:203], v[104:107]
	v_mfma_f32_16x16x128_f8f6f4 v[108:111], v[154:161], v[196:203], v[108:111]
	v_mfma_f32_16x16x128_f8f6f4 v[112:115], v[146:153], v[232:239], v[112:115]
	v_mfma_f32_16x16x128_f8f6f4 v[116:119], v[154:161], v[232:239], v[116:119]
	v_mfma_f32_16x16x128_f8f6f4 v[120:123], v[146:153], v[240:247], v[120:123]
	v_mfma_f32_16x16x128_f8f6f4 v[124:127], v[154:161], v[240:247], v[124:127]
	s_setprio 0
	s_barrier
	s_add_i32 s42, s42, 2
	s_add_u32 s36, s36, 0x100
	s_addc_u32 s37, s37, 0
	s_cmp_gt_u32 s42, 13
	s_cbranch_scc1 .LBB0_914

.LBB0_1008:
	s_add_u32 s5, s38, 0x100
	s_addc_u32 s27, s39, 0
	s_lshl_b32 s44, s61, 8
	s_lshl_b32 s29, s61, 19
	s_bitset1_b32 s44, 7
	s_mov_b32 s45, -2
	s_mov_b64 s[38:39], 0
	s_cmp_eq_u32 s45, 12
	s_cselect_b64 s[42:43], -1, 0
	s_and_b64 s[40:41], s[36:37], s[42:43]
	s_andn2_b64 vcc, exec, s[40:41]
	v_mov_b32_e32 v131, v138
	v_mov_b32_e32 v133, v128
	v_add_u32_e32 v135, s58, v142
	s_add_u32 s64, s6, s38
	v_add_u32_e32 v137, s58, v143
	ds_read_b128 v[178:181], v135
	ds_read_b128 v[186:189], v135 offset:2048
	ds_read_b128 v[182:185], v137
	ds_read_b128 v[190:193], v137 offset:2048
	v_add_u32_e32 v135, s59, v142
	s_addc_u32 s65, s7, s39
	v_add_u32_e32 v137, s59, v143
	ds_read_b128 v[194:197], v135
	ds_read_b128 v[202:205], v135 offset:2048
	ds_read_b128 v[198:201], v137
	ds_read_b128 v[206:209], v137 offset:2048
	s_add_u32 s66, s64, 0x5e000100
	s_addc_u32 s67, s65, 0
	s_and_b64 s[40:41], s[42:43], exec
	s_cselect_b32 s41, s11, s67
	s_cselect_b32 s40, s10, s66
	s_add_u32 s66, s5, s38
	s_addc_u32 s67, s27, s39
	s_and_b64 s[42:43], s[42:43], exec
	s_cselect_b32 s43, s35, s67
	s_cselect_b32 s42, s34, s66
	ds_read_b128 v[210:213], v175
	ds_read_b128 v[218:221], v175 offset:2048
	ds_read_b128 v[214:217], v176
	ds_read_b128 v[222:225], v176 offset:2048
	ds_read_b128 v[226:229], v175 offset:4096
	ds_read_b128 v[234:237], v175 offset:6144
	ds_read_b128 v[230:233], v176 offset:4096
	ds_read_b128 v[238:241], v176 offset:6144
	s_add_i32 m0, s1, 0xc000
	s_add_u32 vcc_lo, s64, s16
	s_addc_u32 vcc_hi, s65, s17
	global_load_lds_dwordx4 v128, vcc
	v_mov_b32_e32 v139, v129
	s_add_i32 m0, s1, 0xe000
	s_nop 0
	global_load_lds_dwordx4 v138, vcc
	s_waitcnt vmcnt(8)
	s_waitcnt lgkmcnt(0)
	s_barrier
	s_setprio 1
	s_waitcnt lgkmcnt(0)
	v_mfma_f32_16x16x128_f8f6f4 v[100:103], v[178:185], v[210:217], 0
	v_mfma_f32_16x16x128_f8f6f4 v[96:99], v[186:193], v[210:217], 0
	v_mfma_f32_16x16x128_f8f6f4 v[92:95], v[178:185], v[218:225], 0
	v_mfma_f32_16x16x128_f8f6f4 v[88:91], v[186:193], v[218:225], 0
	v_mfma_f32_16x16x128_f8f6f4 v[84:87], v[178:185], v[226:233], 0
	v_mfma_f32_16x16x128_f8f6f4 v[80:83], v[186:193], v[226:233], 0
	v_mfma_f32_16x16x128_f8f6f4 v[242:245], v[178:185], v[234:241], 0
	v_mfma_f32_16x16x128_f8f6f4 v[246:249], v[186:193], v[234:241], 0
	s_setprio 0
	s_setprio 1
	v_mfma_f32_16x16x128_f8f6f4 v[40:43], v[194:201], v[234:241], 0
	v_mfma_f32_16x16x128_f8f6f4 v[32:35], v[202:209], v[234:241], 0
	v_mfma_f32_16x16x128_f8f6f4 v[250:253], v[194:201], v[210:217], 0
	v_mfma_f32_16x16x128_f8f6f4 v[144:147], v[202:209], v[210:217], 0
	v_mfma_f32_16x16x128_f8f6f4 v[148:151], v[194:201], v[218:225], 0
	v_mfma_f32_16x16x128_f8f6f4 v[152:155], v[202:209], v[218:225], 0
	v_mfma_f32_16x16x128_f8f6f4 v[156:159], v[194:201], v[226:233], 0
	v_mfma_f32_16x16x128_f8f6f4 v[160:163], v[202:209], v[226:233], 0
	s_setprio 0
	s_barrier
	s_add_i32 s64, s58, s48
	s_mov_b32 m0, s64
	s_nop 2
	s_nop 0
	global_load_lds_dwordx4 v136, s[42:43]
	s_add_i32 m0, s64, 0x2000
	s_add_u32 s64, s42, 0x4000
	s_addc_u32 s65, s43, 0
	s_add_i32 s66, s59, s48
	s_nop 0
	global_load_lds_dwordx4 v130, s[42:43]
	s_mov_b32 m0, s66
	s_nop 0
	global_load_lds_dwordx4 v136, s[64:65]
	s_add_i32 m0, s66, 0x2000
	s_nop 0
	global_load_lds_dwordx4 v130, s[64:65]
	ds_read_b128 v[48:51], v175 offset:16384
	ds_read_b128 v[56:59], v175 offset:18432
	ds_read_b128 v[52:55], v176 offset:16384
	ds_read_b128 v[60:63], v176 offset:18432
	ds_read_b128 v[64:67], v175 offset:20480
	ds_read_b128 v[72:75], v175 offset:22528
	ds_read_b128 v[68:71], v176 offset:20480
	ds_read_b128 v[76:79], v176 offset:22528
	s_waitcnt vmcnt(6)
	s_waitcnt lgkmcnt(0)
	s_barrier
	s_setprio 1
	s_waitcnt lgkmcnt(0)
	v_mfma_f32_16x16x128_f8f6f4 v[44:47], v[178:185], v[48:55], 0
	v_mfma_f32_16x16x128_f8f6f4 v[36:39], v[186:193], v[48:55], 0
	v_mfma_f32_16x16x128_f8f6f4 v[28:31], v[178:185], v[56:63], 0
	v_mfma_f32_16x16x128_f8f6f4 v[24:27], v[186:193], v[56:63], 0
	v_mfma_f32_16x16x128_f8f6f4 v[20:23], v[178:185], v[64:71], 0
	v_mfma_f32_16x16x128_f8f6f4 v[16:19], v[186:193], v[64:71], 0
	v_mfma_f32_16x16x128_f8f6f4 v[12:15], v[178:185], v[72:79], 0
	v_mfma_f32_16x16x128_f8f6f4 v[8:11], v[186:193], v[72:79], 0
	s_setprio 0
	s_setprio 1
	v_mfma_f32_16x16x128_f8f6f4 v[4:7], v[194:201], v[48:55], 0
	v_mfma_f32_16x16x128_f8f6f4 v[0:3], v[202:209], v[48:55], 0
	v_mfma_f32_16x16x128_f8f6f4 v[104:107], v[194:201], v[56:63], 0
	v_mfma_f32_16x16x128_f8f6f4 v[108:111], v[202:209], v[56:63], 0
	v_mfma_f32_16x16x128_f8f6f4 v[112:115], v[194:201], v[64:71], 0
	v_mfma_f32_16x16x128_f8f6f4 v[116:119], v[202:209], v[64:71], 0
	v_mfma_f32_16x16x128_f8f6f4 v[120:123], v[194:201], v[72:79], 0
	v_mfma_f32_16x16x128_f8f6f4 v[124:127], v[202:209], v[72:79], 0
	s_setprio 0
	s_barrier
	s_add_i32 s64, 0, 0x18000
	v_add_u32_e32 v48, s64, v142
	s_add_i32 s65, 0, 0x1c000
	v_add_u32_e32 v49, s64, v143
	ds_read_b128 v[178:181], v48
	ds_read_b128 v[186:189], v48 offset:2048
	ds_read_b128 v[182:185], v49
	ds_read_b128 v[190:193], v49 offset:2048
	v_add_u32_e32 v48, s65, v142
	v_add_u32_e32 v49, s65, v143
	ds_read_b128 v[194:197], v48
	ds_read_b128 v[202:205], v48 offset:2048
	ds_read_b128 v[198:201], v49
	ds_read_b128 v[206:209], v49 offset:2048
	s_mov_b32 m0, s50
	v_mov_b32_e32 v128, v133
	ds_read_b128 v[48:51], v175 offset:32768
	ds_read_b128 v[210:213], v175 offset:34816
	ds_read_b128 v[52:55], v176 offset:32768
	ds_read_b128 v[214:217], v176 offset:34816
	ds_read_b128 v[218:221], v175 offset:36864
	ds_read_b128 v[226:229], v175 offset:38912
	ds_read_b128 v[222:225], v176 offset:36864
	ds_read_b128 v[230:233], v176 offset:38912
	s_mov_b32 m0, s1
	s_nop 0
	global_load_lds_dwordx4 v132, s[40:41]
	s_mov_b32 m0, s49
	s_nop 0
	global_load_lds_dwordx4 v134, s[40:41]
	s_mov_b32 m0, s50
	v_mov_b32_e32 v138, v131
	global_load_lds_dwordx4 v128, s[40:41]
	s_mov_b32 m0, s51
	s_nop 0
	global_load_lds_dwordx4 v138, s[40:41]
	s_waitcnt vmcnt(8)
	s_waitcnt lgkmcnt(0)
	s_barrier
	s_setprio 1
	s_waitcnt lgkmcnt(0)
	v_mfma_f32_16x16x128_f8f6f4 v[100:103], v[178:185], v[48:55], v[100:103]
	v_mfma_f32_16x16x128_f8f6f4 v[96:99], v[186:193], v[48:55], v[96:99]
	v_mfma_f32_16x16x128_f8f6f4 v[92:95], v[178:185], v[210:217], v[92:95]
	v_mfma_f32_16x16x128_f8f6f4 v[88:91], v[186:193], v[210:217], v[88:91]
	v_mfma_f32_16x16x128_f8f6f4 v[84:87], v[178:185], v[218:225], v[84:87]
	v_mfma_f32_16x16x128_f8f6f4 v[80:83], v[186:193], v[218:225], v[80:83]
	v_mfma_f32_16x16x128_f8f6f4 v[76:79], v[178:185], v[226:233], v[242:245]
	v_mfma_f32_16x16x128_f8f6f4 v[72:75], v[186:193], v[226:233], v[246:249]
	s_setprio 0
	s_setprio 1
	v_mfma_f32_16x16x128_f8f6f4 v[68:71], v[194:201], v[48:55], v[250:253]
	v_mfma_f32_16x16x128_f8f6f4 v[64:67], v[202:209], v[48:55], v[144:147]
	v_mfma_f32_16x16x128_f8f6f4 v[60:63], v[194:201], v[210:217], v[148:151]
	v_mfma_f32_16x16x128_f8f6f4 v[56:59], v[202:209], v[210:217], v[152:155]
	v_mfma_f32_16x16x128_f8f6f4 v[52:55], v[194:201], v[218:225], v[156:159]
	v_mfma_f32_16x16x128_f8f6f4 v[48:51], v[202:209], v[218:225], v[160:163]
	v_mfma_f32_16x16x128_f8f6f4 v[40:43], v[194:201], v[226:233], v[40:43]
	v_mfma_f32_16x16x128_f8f6f4 v[32:35], v[202:209], v[226:233], v[32:35]
	s_setprio 0
	s_barrier
	v_mov_b32_e32 v137, v129
	s_add_i32 s64, s64, s48
	s_add_u32 vcc_lo, s42, s14
	s_addc_u32 vcc_hi, s43, s15
	s_mov_b32 m0, s64
	v_mov_b32_e32 v131, v129
	global_load_lds_dwordx4 v136, vcc
	s_add_i32 m0, s64, 0x2000
	v_mov_b32_e32 v133, v129
	s_add_u32 s42, s42, 0x4080
	s_addc_u32 s43, s43, 0
	s_add_i32 s64, s65, s48
	global_load_lds_dwordx4 v130, vcc
	s_mov_b32 m0, s64
	v_mov_b32_e32 v135, v129
	global_load_lds_dwordx4 v136, s[42:43]
	s_add_i32 m0, s64, 0x2000
	s_nop 0
	global_load_lds_dwordx4 v130, s[42:43]
	s_mov_b32 m0, s53
	s_add_u32 vcc_lo, s40, s14
	s_addc_u32 vcc_hi, s41, s15
	global_load_lds_dwordx4 v132, vcc
	s_mov_b32 m0, s54
	s_nop 0
	global_load_lds_dwordx4 v134, vcc
	ds_read_b128 v[210:213], v175 offset:49152
	ds_read_b128 v[218:221], v175 offset:51200
	ds_read_b128 v[214:217], v176 offset:49152
	ds_read_b128 v[222:225], v176 offset:51200
	ds_read_b128 v[226:229], v175 offset:53248
	ds_read_b128 v[234:237], v175 offset:55296
	ds_read_b128 v[230:233], v176 offset:53248
	ds_read_b128 v[238:241], v176 offset:55296
	s_waitcnt vmcnt(8)
	s_waitcnt lgkmcnt(0)
	s_barrier
	s_setprio 1
	s_waitcnt lgkmcnt(0)
	v_mfma_f32_16x16x128_f8f6f4 v[44:47], v[178:185], v[210:217], v[44:47]
	v_mfma_f32_16x16x128_f8f6f4 v[36:39], v[186:193], v[210:217], v[36:39]
	v_mfma_f32_16x16x128_f8f6f4 v[28:31], v[178:185], v[218:225], v[28:31]
	v_mfma_f32_16x16x128_f8f6f4 v[24:27], v[186:193], v[218:225], v[24:27]
	v_mfma_f32_16x16x128_f8f6f4 v[20:23], v[178:185], v[226:233], v[20:23]
	v_mfma_f32_16x16x128_f8f6f4 v[16:19], v[186:193], v[226:233], v[16:19]
	v_mfma_f32_16x16x128_f8f6f4 v[12:15], v[178:185], v[234:241], v[12:15]
	v_mfma_f32_16x16x128_f8f6f4 v[8:11], v[186:193], v[234:241], v[8:11]
	s_setprio 0
	s_setprio 1
	v_mfma_f32_16x16x128_f8f6f4 v[4:7], v[194:201], v[210:217], v[4:7]
	v_mfma_f32_16x16x128_f8f6f4 v[0:3], v[202:209], v[210:217], v[0:3]
	v_mfma_f32_16x16x128_f8f6f4 v[104:107], v[194:201], v[218:225], v[104:107]
	v_mfma_f32_16x16x128_f8f6f4 v[108:111], v[202:209], v[218:225], v[108:111]
	v_mfma_f32_16x16x128_f8f6f4 v[112:115], v[194:201], v[226:233], v[112:115]
	v_mfma_f32_16x16x128_f8f6f4 v[116:119], v[202:209], v[226:233], v[116:119]
	v_mfma_f32_16x16x128_f8f6f4 v[120:123], v[194:201], v[234:241], v[120:123]
	v_mfma_f32_16x16x128_f8f6f4 v[124:127], v[202:209], v[234:241], v[124:127]
	s_setprio 0
	s_barrier
	s_add_i32 s45, s45, 2
	s_add_u32 s38, s38, 0x100
	s_addc_u32 s39, s39, 0
	s_branch .LBB0_1010
.LBB0_1009:
	v_add_u32_e32 v135, s58, v142
	s_add_u32 s64, s6, s38
	v_add_u32_e32 v137, s58, v143
	ds_read_b128 v[178:181], v135
	ds_read_b128 v[186:189], v135 offset:2048
	ds_read_b128 v[182:185], v137
	ds_read_b128 v[190:193], v137 offset:2048
	v_add_u32_e32 v135, s59, v142
	s_addc_u32 s65, s7, s39
	v_add_u32_e32 v137, s59, v143
	ds_read_b128 v[194:197], v135
	ds_read_b128 v[202:205], v135 offset:2048
	ds_read_b128 v[198:201], v137
	ds_read_b128 v[206:209], v137 offset:2048
	s_add_u32 s66, s64, 0x5e000100
	s_addc_u32 s67, s65, 0
	s_and_b64 s[40:41], s[42:43], exec
	s_cselect_b32 s41, s11, s67
	s_cselect_b32 s40, s10, s66
	s_add_u32 s66, s5, s38
	s_addc_u32 s67, s27, s39
	s_and_b64 s[42:43], s[42:43], exec
	s_cselect_b32 s43, s35, s67
	s_cselect_b32 s42, s34, s66
	ds_read_b128 v[210:213], v175
	ds_read_b128 v[218:221], v175 offset:2048
	ds_read_b128 v[214:217], v176
	ds_read_b128 v[222:225], v176 offset:2048
	ds_read_b128 v[226:229], v175 offset:4096
	ds_read_b128 v[234:237], v175 offset:6144
	ds_read_b128 v[230:233], v176 offset:4096
	ds_read_b128 v[238:241], v176 offset:6144
	s_add_i32 m0, s1, 0xc000
	s_add_u32 vcc_lo, s64, s16
	s_addc_u32 vcc_hi, s65, s17
	global_load_lds_dwordx4 v128, vcc
	v_mov_b32_e32 v139, v129
	s_add_i32 m0, s1, 0xe000
	s_nop 0
	global_load_lds_dwordx4 v138, vcc
	s_waitcnt vmcnt(8)
	s_waitcnt lgkmcnt(0)
	s_barrier
	s_setprio 1
	s_waitcnt lgkmcnt(0)
	v_mfma_f32_16x16x128_f8f6f4 v[100:103], v[178:185], v[210:217], v[100:103]
	v_mfma_f32_16x16x128_f8f6f4 v[96:99], v[186:193], v[210:217], v[96:99]
	v_mfma_f32_16x16x128_f8f6f4 v[92:95], v[178:185], v[218:225], v[92:95]
	v_mfma_f32_16x16x128_f8f6f4 v[88:91], v[186:193], v[218:225], v[88:91]
	v_mfma_f32_16x16x128_f8f6f4 v[84:87], v[178:185], v[226:233], v[84:87]
	v_mfma_f32_16x16x128_f8f6f4 v[80:83], v[186:193], v[226:233], v[80:83]
	v_mfma_f32_16x16x128_f8f6f4 v[242:245], v[178:185], v[234:241], v[76:79]
	v_mfma_f32_16x16x128_f8f6f4 v[246:249], v[186:193], v[234:241], v[72:75]
	s_setprio 0
	s_setprio 1
	v_mfma_f32_16x16x128_f8f6f4 v[40:43], v[194:201], v[234:241], v[40:43]
	v_mfma_f32_16x16x128_f8f6f4 v[32:35], v[202:209], v[234:241], v[32:35]
	v_mfma_f32_16x16x128_f8f6f4 v[250:253], v[194:201], v[210:217], v[68:71]
	v_mfma_f32_16x16x128_f8f6f4 v[144:147], v[202:209], v[210:217], v[64:67]
	v_mfma_f32_16x16x128_f8f6f4 v[148:151], v[194:201], v[218:225], v[60:63]
	v_mfma_f32_16x16x128_f8f6f4 v[152:155], v[202:209], v[218:225], v[56:59]
	v_mfma_f32_16x16x128_f8f6f4 v[156:159], v[194:201], v[226:233], v[52:55]
	v_mfma_f32_16x16x128_f8f6f4 v[160:163], v[202:209], v[226:233], v[48:51]
	s_setprio 0
	s_barrier
	s_add_i32 s64, s58, s48
	s_mov_b32 m0, s64
	s_nop 2
	s_nop 0
	global_load_lds_dwordx4 v136, s[42:43]
	s_add_i32 m0, s64, 0x2000
	s_add_u32 s64, s42, 0x4000
	s_addc_u32 s65, s43, 0
	s_add_i32 s66, s59, s48
	s_nop 0
	global_load_lds_dwordx4 v130, s[42:43]
	s_mov_b32 m0, s66
	s_nop 0
	global_load_lds_dwordx4 v136, s[64:65]
	s_add_i32 m0, s66, 0x2000
	s_nop 0
	global_load_lds_dwordx4 v130, s[64:65]
	ds_read_b128 v[48:51], v175 offset:16384
	ds_read_b128 v[56:59], v175 offset:18432
	ds_read_b128 v[52:55], v176 offset:16384
	ds_read_b128 v[60:63], v176 offset:18432
	ds_read_b128 v[64:67], v175 offset:20480
	ds_read_b128 v[72:75], v175 offset:22528
	ds_read_b128 v[68:71], v176 offset:20480
	ds_read_b128 v[76:79], v176 offset:22528
	s_waitcnt vmcnt(6)
	s_waitcnt lgkmcnt(0)
	s_barrier
	s_setprio 1
	s_waitcnt lgkmcnt(0)
	v_mfma_f32_16x16x128_f8f6f4 v[44:47], v[178:185], v[48:55], v[44:47]
	v_mfma_f32_16x16x128_f8f6f4 v[36:39], v[186:193], v[48:55], v[36:39]
	v_mfma_f32_16x16x128_f8f6f4 v[28:31], v[178:185], v[56:63], v[28:31]
	v_mfma_f32_16x16x128_f8f6f4 v[24:27], v[186:193], v[56:63], v[24:27]
	v_mfma_f32_16x16x128_f8f6f4 v[20:23], v[178:185], v[64:71], v[20:23]
	v_mfma_f32_16x16x128_f8f6f4 v[16:19], v[186:193], v[64:71], v[16:19]
	v_mfma_f32_16x16x128_f8f6f4 v[12:15], v[178:185], v[72:79], v[12:15]
	v_mfma_f32_16x16x128_f8f6f4 v[8:11], v[186:193], v[72:79], v[8:11]
	s_setprio 0
	s_setprio 1
	v_mfma_f32_16x16x128_f8f6f4 v[4:7], v[194:201], v[48:55], v[4:7]
	v_mfma_f32_16x16x128_f8f6f4 v[0:3], v[202:209], v[48:55], v[0:3]
	v_mfma_f32_16x16x128_f8f6f4 v[104:107], v[194:201], v[56:63], v[104:107]
	v_mfma_f32_16x16x128_f8f6f4 v[108:111], v[202:209], v[56:63], v[108:111]
	v_mfma_f32_16x16x128_f8f6f4 v[112:115], v[194:201], v[64:71], v[112:115]
	v_mfma_f32_16x16x128_f8f6f4 v[116:119], v[202:209], v[64:71], v[116:119]
	v_mfma_f32_16x16x128_f8f6f4 v[120:123], v[194:201], v[72:79], v[120:123]
	v_mfma_f32_16x16x128_f8f6f4 v[124:127], v[202:209], v[72:79], v[124:127]
	s_setprio 0
	s_barrier
	s_add_i32 s64, 0, 0x18000
	v_add_u32_e32 v48, s64, v142
	s_add_i32 s65, 0, 0x1c000
	v_add_u32_e32 v49, s64, v143
	ds_read_b128 v[178:181], v48
	ds_read_b128 v[186:189], v48 offset:2048
	ds_read_b128 v[182:185], v49
	ds_read_b128 v[190:193], v49 offset:2048
	v_add_u32_e32 v48, s65, v142
	v_add_u32_e32 v49, s65, v143
	ds_read_b128 v[194:197], v48
	ds_read_b128 v[202:205], v48 offset:2048
	ds_read_b128 v[198:201], v49
	ds_read_b128 v[206:209], v49 offset:2048
	s_mov_b32 m0, s50
	v_mov_b32_e32 v128, v133
	ds_read_b128 v[48:51], v175 offset:32768
	ds_read_b128 v[210:213], v175 offset:34816
	ds_read_b128 v[52:55], v176 offset:32768
	ds_read_b128 v[214:217], v176 offset:34816
	ds_read_b128 v[218:221], v175 offset:36864
	ds_read_b128 v[226:229], v175 offset:38912
	ds_read_b128 v[222:225], v176 offset:36864
	ds_read_b128 v[230:233], v176 offset:38912
	s_mov_b32 m0, s1
	s_nop 0
	global_load_lds_dwordx4 v132, s[40:41]
	s_mov_b32 m0, s49
	s_nop 0
	global_load_lds_dwordx4 v134, s[40:41]
	s_mov_b32 m0, s50
	v_mov_b32_e32 v138, v131
	global_load_lds_dwordx4 v128, s[40:41]
	s_mov_b32 m0, s51
	s_nop 0
	global_load_lds_dwordx4 v138, s[40:41]
	s_waitcnt vmcnt(8)
	s_waitcnt lgkmcnt(0)
	s_barrier
	s_setprio 1
	s_waitcnt lgkmcnt(0)
	v_mfma_f32_16x16x128_f8f6f4 v[100:103], v[178:185], v[48:55], v[100:103]
	v_mfma_f32_16x16x128_f8f6f4 v[96:99], v[186:193], v[48:55], v[96:99]
	v_mfma_f32_16x16x128_f8f6f4 v[92:95], v[178:185], v[210:217], v[92:95]
	v_mfma_f32_16x16x128_f8f6f4 v[88:91], v[186:193], v[210:217], v[88:91]
	v_mfma_f32_16x16x128_f8f6f4 v[84:87], v[178:185], v[218:225], v[84:87]
	v_mfma_f32_16x16x128_f8f6f4 v[80:83], v[186:193], v[218:225], v[80:83]
	v_mfma_f32_16x16x128_f8f6f4 v[76:79], v[178:185], v[226:233], v[242:245]
	v_mfma_f32_16x16x128_f8f6f4 v[72:75], v[186:193], v[226:233], v[246:249]
	s_setprio 0
	s_setprio 1
	v_mfma_f32_16x16x128_f8f6f4 v[68:71], v[194:201], v[48:55], v[250:253]
	v_mfma_f32_16x16x128_f8f6f4 v[64:67], v[202:209], v[48:55], v[144:147]
	v_mfma_f32_16x16x128_f8f6f4 v[60:63], v[194:201], v[210:217], v[148:151]
	v_mfma_f32_16x16x128_f8f6f4 v[56:59], v[202:209], v[210:217], v[152:155]
	v_mfma_f32_16x16x128_f8f6f4 v[52:55], v[194:201], v[218:225], v[156:159]
	v_mfma_f32_16x16x128_f8f6f4 v[48:51], v[202:209], v[218:225], v[160:163]
	v_mfma_f32_16x16x128_f8f6f4 v[40:43], v[194:201], v[226:233], v[40:43]
	v_mfma_f32_16x16x128_f8f6f4 v[32:35], v[202:209], v[226:233], v[32:35]
	s_setprio 0
	s_barrier
	v_mov_b32_e32 v137, v129
	s_add_i32 s64, s64, s48
	s_add_u32 vcc_lo, s42, s14
	s_addc_u32 vcc_hi, s43, s15
	s_mov_b32 m0, s64
	v_mov_b32_e32 v131, v129
	global_load_lds_dwordx4 v136, vcc
	s_add_i32 m0, s64, 0x2000
	v_mov_b32_e32 v133, v129
	s_add_u32 s42, s42, 0x4080
	s_addc_u32 s43, s43, 0
	s_add_i32 s64, s65, s48
	global_load_lds_dwordx4 v130, vcc
	s_mov_b32 m0, s64
	v_mov_b32_e32 v135, v129
	global_load_lds_dwordx4 v136, s[42:43]
	s_add_i32 m0, s64, 0x2000
	s_nop 0
	global_load_lds_dwordx4 v130, s[42:43]
	s_mov_b32 m0, s53
	s_add_u32 vcc_lo, s40, s14
	s_addc_u32 vcc_hi, s41, s15
	global_load_lds_dwordx4 v132, vcc
	s_mov_b32 m0, s54
	s_nop 0
	global_load_lds_dwordx4 v134, vcc
	ds_read_b128 v[210:213], v175 offset:49152
	ds_read_b128 v[218:221], v175 offset:51200
	ds_read_b128 v[214:217], v176 offset:49152
	ds_read_b128 v[222:225], v176 offset:51200
	ds_read_b128 v[226:229], v175 offset:53248
	ds_read_b128 v[234:237], v175 offset:55296
	ds_read_b128 v[230:233], v176 offset:53248
	ds_read_b128 v[238:241], v176 offset:55296
	s_waitcnt vmcnt(8)
	s_waitcnt lgkmcnt(0)
	s_barrier
	s_setprio 1
	s_waitcnt lgkmcnt(0)
	v_mfma_f32_16x16x128_f8f6f4 v[44:47], v[178:185], v[210:217], v[44:47]
	v_mfma_f32_16x16x128_f8f6f4 v[36:39], v[186:193], v[210:217], v[36:39]
	v_mfma_f32_16x16x128_f8f6f4 v[28:31], v[178:185], v[218:225], v[28:31]
	v_mfma_f32_16x16x128_f8f6f4 v[24:27], v[186:193], v[218:225], v[24:27]
	v_mfma_f32_16x16x128_f8f6f4 v[20:23], v[178:185], v[226:233], v[20:23]
	v_mfma_f32_16x16x128_f8f6f4 v[16:19], v[186:193], v[226:233], v[16:19]
	v_mfma_f32_16x16x128_f8f6f4 v[12:15], v[178:185], v[234:241], v[12:15]
	v_mfma_f32_16x16x128_f8f6f4 v[8:11], v[186:193], v[234:241], v[8:11]
	s_setprio 0
	s_setprio 1
	v_mfma_f32_16x16x128_f8f6f4 v[4:7], v[194:201], v[210:217], v[4:7]
	v_mfma_f32_16x16x128_f8f6f4 v[0:3], v[202:209], v[210:217], v[0:3]
	v_mfma_f32_16x16x128_f8f6f4 v[104:107], v[194:201], v[218:225], v[104:107]
	v_mfma_f32_16x16x128_f8f6f4 v[108:111], v[202:209], v[218:225], v[108:111]
	v_mfma_f32_16x16x128_f8f6f4 v[112:115], v[194:201], v[226:233], v[112:115]
	v_mfma_f32_16x16x128_f8f6f4 v[116:119], v[202:209], v[226:233], v[116:119]
	v_mfma_f32_16x16x128_f8f6f4 v[120:123], v[194:201], v[234:241], v[120:123]
	v_mfma_f32_16x16x128_f8f6f4 v[124:127], v[202:209], v[234:241], v[124:127]
	s_setprio 0
	s_barrier
	s_add_i32 s45, s45, 2
	s_add_u32 s38, s38, 0x100
	s_addc_u32 s39, s39, 0
	s_cmp_gt_u32 s45, 13
	s_cbranch_scc1 .LBB0_1012
